# combination on v071: peeled last K iteration in MoE loops, converter counted waits re-derived (no store-ack wait per half), ticket read before the output stores, batched xn2 conversion in the router
# speedup vs baseline: 1.0112x; 1.0084x over previous
; __device__ __forceinline__ void phase_router(const Params& p, LAS3 char* lds, int wid) {
;     ...
; #pragma unroll 1
;         for (int q = 0; q < 4; ++q) {
;             const int tk = wid * 4 + q;
;             const float r = rstd[tk];
;             const float* hr = p.h + (size_t)(t0 + tk) * D;
; #pragma unroll
;             for (int j = 0; j < 8; ++j) {
;                 const f32x4 hv = *(const f32x4*)(hr + j * 256 + lane * 4), gg = *(const f32x4*)(p.ln_ffn_g + j * 256 + lane * 4);
;                 int o = __builtin_amdgcn_cvt_pk_fp8_f32(hv[0] * r * gg[0], hv[1] * r * gg[1], 0, false);
;                 o = __builtin_amdgcn_cvt_pk_fp8_f32(hv[2] * r * gg[2], hv[3] * r * gg[3], o, true);
;                 *(int*)((unsigned char*)p.xn2 + (size_t)(t0 + tk) * D + j * 256 + lane * 4) = o;
;             }
;         }
.LBB0_352:
	global_load_dwordx4 v[106:109], v[36:37], off
	global_load_dwordx4 v[110:113], v[36:37], off offset:1024
	global_load_dwordx4 v[114:117], v[36:37], off offset:2048
	global_load_dwordx4 v[118:121], v[36:37], off offset:3072
	global_load_dwordx4 v[122:125], v[38:39], off
	global_load_dwordx4 v[126:129], v[40:41], off
	global_load_dwordx4 v[130:133], v[42:43], off
	global_load_dwordx4 v[134:137], v[44:45], off
	v_mov_b32_e32 v238, s18
	ds_read_b32 v234, v238
	ds_read_b32 v235, v238 offset:4
	ds_read_b32 v236, v238 offset:8
	ds_read_b32 v237, v238 offset:12
	v_mov_b64_e32 v[244:245], v[0:1]
	s_mov_b64 s[26:27], 0x1000
	v_lshl_add_u64 v[246:247], v[0:1], 0, s[26:27]
	global_load_dwordx4 v[138:141], v[244:245], off
	global_load_dwordx4 v[142:145], v[244:245], off offset:1024
	global_load_dwordx4 v[146:149], v[244:245], off offset:2048
	global_load_dwordx4 v[150:153], v[244:245], off offset:3072
	global_load_dwordx4 v[154:157], v[246:247], off
	global_load_dwordx4 v[158:161], v[246:247], off offset:1024
	global_load_dwordx4 v[162:165], v[246:247], off offset:2048
	global_load_dwordx4 v[166:169], v[246:247], off offset:3072
	s_mov_b64 s[26:27], 0x2000
	v_lshl_add_u64 v[244:245], v[0:1], 0, s[26:27]
	s_mov_b64 s[26:27], 0x3000
	v_lshl_add_u64 v[246:247], v[0:1], 0, s[26:27]
	global_load_dwordx4 v[170:173], v[244:245], off
	global_load_dwordx4 v[174:177], v[244:245], off offset:1024
	global_load_dwordx4 v[178:181], v[244:245], off offset:2048
	global_load_dwordx4 v[182:185], v[244:245], off offset:3072
	global_load_dwordx4 v[186:189], v[246:247], off
	global_load_dwordx4 v[190:193], v[246:247], off offset:1024
	global_load_dwordx4 v[194:197], v[246:247], off offset:2048
	global_load_dwordx4 v[198:201], v[246:247], off offset:3072
	s_mov_b64 s[26:27], 0x4000
	v_lshl_add_u64 v[244:245], v[0:1], 0, s[26:27]
	s_mov_b64 s[26:27], 0x5000
	v_lshl_add_u64 v[246:247], v[0:1], 0, s[26:27]
	global_load_dwordx4 v[202:205], v[244:245], off
	global_load_dwordx4 v[206:209], v[244:245], off offset:1024
	global_load_dwordx4 v[210:213], v[244:245], off offset:2048
	global_load_dwordx4 v[214:217], v[244:245], off offset:3072
	global_load_dwordx4 v[218:221], v[246:247], off
	global_load_dwordx4 v[222:225], v[246:247], off offset:1024
	global_load_dwordx4 v[226:229], v[246:247], off offset:2048
	global_load_dwordx4 v[230:233], v[246:247], off offset:3072
	s_waitcnt vmcnt(16) lgkmcnt(0)
	v_mov_b64_e32 v[248:249], v[2:3]
	v_mov_b32_e32 v242, 0
	v_mul_f32_e32 v238, v234, v138
	v_mul_f32_e32 v239, v234, v139
	v_mul_f32_e32 v238, v238, v106
	v_mul_f32_e32 v239, v239, v107
	v_cvt_pk_fp8_f32 v242, v238, v239
	v_mul_f32_e32 v240, v234, v140
	v_mul_f32_e32 v241, v234, v141
	v_mul_f32_e32 v240, v240, v108
	v_mul_f32_e32 v241, v241, v109
	v_cvt_pk_fp8_f32 v242, v240, v241 op_sel:[0,0,1]
	global_store_dword v[248:249], v242, off offset:-1024
	v_mov_b32_e32 v242, 0
	v_mul_f32_e32 v238, v234, v142
	v_mul_f32_e32 v239, v234, v143
	v_mul_f32_e32 v238, v238, v110
	v_mul_f32_e32 v239, v239, v111
	v_cvt_pk_fp8_f32 v242, v238, v239
	v_mul_f32_e32 v240, v234, v144
	v_mul_f32_e32 v241, v234, v145
	v_mul_f32_e32 v240, v240, v112
	v_mul_f32_e32 v241, v241, v113
	v_cvt_pk_fp8_f32 v242, v240, v241 op_sel:[0,0,1]
	global_store_dword v[248:249], v242, off offset:-768
	v_mov_b32_e32 v242, 0
	v_mul_f32_e32 v238, v234, v146
	v_mul_f32_e32 v239, v234, v147
	v_mul_f32_e32 v238, v238, v114
	v_mul_f32_e32 v239, v239, v115
	v_cvt_pk_fp8_f32 v242, v238, v239
	v_mul_f32_e32 v240, v234, v148
	v_mul_f32_e32 v241, v234, v149
	v_mul_f32_e32 v240, v240, v116
	v_mul_f32_e32 v241, v241, v117
	v_cvt_pk_fp8_f32 v242, v240, v241 op_sel:[0,0,1]
	global_store_dword v[248:249], v242, off offset:-512
	v_mov_b32_e32 v242, 0
	v_mul_f32_e32 v238, v234, v150
	v_mul_f32_e32 v239, v234, v151
	v_mul_f32_e32 v238, v238, v118
	v_mul_f32_e32 v239, v239, v119
	v_cvt_pk_fp8_f32 v242, v238, v239
	v_mul_f32_e32 v240, v234, v152
	v_mul_f32_e32 v241, v234, v153
	v_mul_f32_e32 v240, v240, v120
	v_mul_f32_e32 v241, v241, v121
	v_cvt_pk_fp8_f32 v242, v240, v241 op_sel:[0,0,1]
	global_store_dword v[248:249], v242, off offset:-256
	v_mov_b32_e32 v242, 0
	v_mul_f32_e32 v238, v234, v154
	v_mul_f32_e32 v239, v234, v155
	v_mul_f32_e32 v238, v238, v122
	v_mul_f32_e32 v239, v239, v123
	v_cvt_pk_fp8_f32 v242, v238, v239
	v_mul_f32_e32 v240, v234, v156
	v_mul_f32_e32 v241, v234, v157
	v_mul_f32_e32 v240, v240, v124
	v_mul_f32_e32 v241, v241, v125
	v_cvt_pk_fp8_f32 v242, v240, v241 op_sel:[0,0,1]
	global_store_dword v[248:249], v242, off
	v_mov_b32_e32 v242, 0
	v_mul_f32_e32 v238, v234, v158
	v_mul_f32_e32 v239, v234, v159
	v_mul_f32_e32 v238, v238, v126
	v_mul_f32_e32 v239, v239, v127
	v_cvt_pk_fp8_f32 v242, v238, v239
	v_mul_f32_e32 v240, v234, v160
	v_mul_f32_e32 v241, v234, v161
	v_mul_f32_e32 v240, v240, v128
	v_mul_f32_e32 v241, v241, v129
	v_cvt_pk_fp8_f32 v242, v240, v241 op_sel:[0,0,1]
	global_store_dword v[248:249], v242, off offset:256
	v_mov_b32_e32 v242, 0
	v_mul_f32_e32 v238, v234, v162
	v_mul_f32_e32 v239, v234, v163
	v_mul_f32_e32 v238, v238, v130
	v_mul_f32_e32 v239, v239, v131
	v_cvt_pk_fp8_f32 v242, v238, v239
	v_mul_f32_e32 v240, v234, v164
	v_mul_f32_e32 v241, v234, v165
	v_mul_f32_e32 v240, v240, v132
	v_mul_f32_e32 v241, v241, v133
	v_cvt_pk_fp8_f32 v242, v240, v241 op_sel:[0,0,1]
	global_store_dword v[248:249], v242, off offset:512
	v_mov_b32_e32 v242, 0
	v_mul_f32_e32 v238, v234, v166
	v_mul_f32_e32 v239, v234, v167
	v_mul_f32_e32 v238, v238, v134
	v_mul_f32_e32 v239, v239, v135
	v_cvt_pk_fp8_f32 v242, v238, v239
	v_mul_f32_e32 v240, v234, v168
	v_mul_f32_e32 v241, v234, v169
	v_mul_f32_e32 v240, v240, v136
	v_mul_f32_e32 v241, v241, v137
	v_cvt_pk_fp8_f32 v242, v240, v241 op_sel:[0,0,1]
	global_store_dword v[248:249], v242, off offset:768
	s_mov_b64 s[26:27], 0x6000
	v_lshl_add_u64 v[244:245], v[0:1], 0, s[26:27]
	s_mov_b64 s[26:27], 0x7000
	v_lshl_add_u64 v[246:247], v[0:1], 0, s[26:27]
	global_load_dwordx4 v[138:141], v[244:245], off
	global_load_dwordx4 v[142:145], v[244:245], off offset:1024
	global_load_dwordx4 v[146:149], v[244:245], off offset:2048
	global_load_dwordx4 v[150:153], v[244:245], off offset:3072
	global_load_dwordx4 v[154:157], v[246:247], off
	global_load_dwordx4 v[158:161], v[246:247], off offset:1024
	global_load_dwordx4 v[162:165], v[246:247], off offset:2048
	global_load_dwordx4 v[166:169], v[246:247], off offset:3072
	s_waitcnt vmcnt(24)
; __device__ __forceinline__ void phase_router(const Params& p, LAS3 char* lds, int wid) {
;     ...
; #pragma unroll 1
;         for (int q = 0; q < 4; ++q) {
;             const int tk = wid * 4 + q;
;             const float r = rstd[tk];
;             const float* hr = p.h + (size_t)(t0 + tk) * D;
; #pragma unroll
;             for (int j = 0; j < 8; ++j) {
;                 const f32x4 hv = *(const f32x4*)(hr + j * 256 + lane * 4), gg = *(const f32x4*)(p.ln_ffn_g + j * 256 + lane * 4);
;                 int o = __builtin_amdgcn_cvt_pk_fp8_f32(hv[0] * r * gg[0], hv[1] * r * gg[1], 0, false);
;                 o = __builtin_amdgcn_cvt_pk_fp8_f32(hv[2] * r * gg[2], hv[3] * r * gg[3], o, true);
;                 *(int*)((unsigned char*)p.xn2 + (size_t)(t0 + tk) * D + j * 256 + lane * 4) = o;
;             }
;         }
	s_mov_b64 s[26:27], 0x800
	v_lshl_add_u64 v[248:249], v[2:3], 0, s[26:27]
	v_mov_b32_e32 v242, 0
	v_mul_f32_e32 v238, v235, v170
	v_mul_f32_e32 v239, v235, v171
	v_mul_f32_e32 v238, v238, v106
	v_mul_f32_e32 v239, v239, v107
	v_cvt_pk_fp8_f32 v242, v238, v239
	v_mul_f32_e32 v240, v235, v172
	v_mul_f32_e32 v241, v235, v173
	v_mul_f32_e32 v240, v240, v108
	v_mul_f32_e32 v241, v241, v109
	v_cvt_pk_fp8_f32 v242, v240, v241 op_sel:[0,0,1]
	global_store_dword v[248:249], v242, off offset:-1024
	v_mov_b32_e32 v242, 0
	v_mul_f32_e32 v238, v235, v174
	v_mul_f32_e32 v239, v235, v175
	v_mul_f32_e32 v238, v238, v110
	v_mul_f32_e32 v239, v239, v111
	v_cvt_pk_fp8_f32 v242, v238, v239
	v_mul_f32_e32 v240, v235, v176
	v_mul_f32_e32 v241, v235, v177
	v_mul_f32_e32 v240, v240, v112
	v_mul_f32_e32 v241, v241, v113
	v_cvt_pk_fp8_f32 v242, v240, v241 op_sel:[0,0,1]
	global_store_dword v[248:249], v242, off offset:-768
	v_mov_b32_e32 v242, 0
	v_mul_f32_e32 v238, v235, v178
	v_mul_f32_e32 v239, v235, v179
	v_mul_f32_e32 v238, v238, v114
	v_mul_f32_e32 v239, v239, v115
	v_cvt_pk_fp8_f32 v242, v238, v239
	v_mul_f32_e32 v240, v235, v180
	v_mul_f32_e32 v241, v235, v181
	v_mul_f32_e32 v240, v240, v116
	v_mul_f32_e32 v241, v241, v117
	v_cvt_pk_fp8_f32 v242, v240, v241 op_sel:[0,0,1]
	global_store_dword v[248:249], v242, off offset:-512
	v_mov_b32_e32 v242, 0
	v_mul_f32_e32 v238, v235, v182
	v_mul_f32_e32 v239, v235, v183
	v_mul_f32_e32 v238, v238, v118
	v_mul_f32_e32 v239, v239, v119
	v_cvt_pk_fp8_f32 v242, v238, v239
	v_mul_f32_e32 v240, v235, v184
	v_mul_f32_e32 v241, v235, v185
	v_mul_f32_e32 v240, v240, v120
	v_mul_f32_e32 v241, v241, v121
	v_cvt_pk_fp8_f32 v242, v240, v241 op_sel:[0,0,1]
	global_store_dword v[248:249], v242, off offset:-256
	v_mov_b32_e32 v242, 0
	v_mul_f32_e32 v238, v235, v186
	v_mul_f32_e32 v239, v235, v187
	v_mul_f32_e32 v238, v238, v122
	v_mul_f32_e32 v239, v239, v123
	v_cvt_pk_fp8_f32 v242, v238, v239
	v_mul_f32_e32 v240, v235, v188
	v_mul_f32_e32 v241, v235, v189
	v_mul_f32_e32 v240, v240, v124
	v_mul_f32_e32 v241, v241, v125
	v_cvt_pk_fp8_f32 v242, v240, v241 op_sel:[0,0,1]
	global_store_dword v[248:249], v242, off
	v_mov_b32_e32 v242, 0
	v_mul_f32_e32 v238, v235, v190
	v_mul_f32_e32 v239, v235, v191
	v_mul_f32_e32 v238, v238, v126
	v_mul_f32_e32 v239, v239, v127
	v_cvt_pk_fp8_f32 v242, v238, v239
	v_mul_f32_e32 v240, v235, v192
	v_mul_f32_e32 v241, v235, v193
	v_mul_f32_e32 v240, v240, v128
	v_mul_f32_e32 v241, v241, v129
	v_cvt_pk_fp8_f32 v242, v240, v241 op_sel:[0,0,1]
	global_store_dword v[248:249], v242, off offset:256
	v_mov_b32_e32 v242, 0
	v_mul_f32_e32 v238, v235, v194
	v_mul_f32_e32 v239, v235, v195
	v_mul_f32_e32 v238, v238, v130
	v_mul_f32_e32 v239, v239, v131
	v_cvt_pk_fp8_f32 v242, v238, v239
	v_mul_f32_e32 v240, v235, v196
	v_mul_f32_e32 v241, v235, v197
	v_mul_f32_e32 v240, v240, v132
	v_mul_f32_e32 v241, v241, v133
	v_cvt_pk_fp8_f32 v242, v240, v241 op_sel:[0,0,1]
	global_store_dword v[248:249], v242, off offset:512
	v_mov_b32_e32 v242, 0
	v_mul_f32_e32 v238, v235, v198
	v_mul_f32_e32 v239, v235, v199
	v_mul_f32_e32 v238, v238, v134
	v_mul_f32_e32 v239, v239, v135
	v_cvt_pk_fp8_f32 v242, v238, v239
	v_mul_f32_e32 v240, v235, v200
	v_mul_f32_e32 v241, v235, v201
	v_mul_f32_e32 v240, v240, v136
	v_mul_f32_e32 v241, v241, v137
	v_cvt_pk_fp8_f32 v242, v240, v241 op_sel:[0,0,1]
	global_store_dword v[248:249], v242, off offset:768
	s_waitcnt vmcnt(24)
	s_mov_b64 s[26:27], 0x1000
	v_lshl_add_u64 v[248:249], v[2:3], 0, s[26:27]
	v_mov_b32_e32 v242, 0
	v_mul_f32_e32 v238, v236, v202
	v_mul_f32_e32 v239, v236, v203
	v_mul_f32_e32 v238, v238, v106
	v_mul_f32_e32 v239, v239, v107
	v_cvt_pk_fp8_f32 v242, v238, v239
	v_mul_f32_e32 v240, v236, v204
	v_mul_f32_e32 v241, v236, v205
	v_mul_f32_e32 v240, v240, v108
	v_mul_f32_e32 v241, v241, v109
	v_cvt_pk_fp8_f32 v242, v240, v241 op_sel:[0,0,1]
	global_store_dword v[248:249], v242, off offset:-1024
	v_mov_b32_e32 v242, 0
	v_mul_f32_e32 v238, v236, v206
	v_mul_f32_e32 v239, v236, v207
	v_mul_f32_e32 v238, v238, v110
	v_mul_f32_e32 v239, v239, v111
	v_cvt_pk_fp8_f32 v242, v238, v239
	v_mul_f32_e32 v240, v236, v208
	v_mul_f32_e32 v241, v236, v209
	v_mul_f32_e32 v240, v240, v112
	v_mul_f32_e32 v241, v241, v113
	v_cvt_pk_fp8_f32 v242, v240, v241 op_sel:[0,0,1]
	global_store_dword v[248:249], v242, off offset:-768
	v_mov_b32_e32 v242, 0
	v_mul_f32_e32 v238, v236, v210
	v_mul_f32_e32 v239, v236, v211
	v_mul_f32_e32 v238, v238, v114
	v_mul_f32_e32 v239, v239, v115
	v_cvt_pk_fp8_f32 v242, v238, v239
	v_mul_f32_e32 v240, v236, v212
	v_mul_f32_e32 v241, v236, v213
	v_mul_f32_e32 v240, v240, v116
	v_mul_f32_e32 v241, v241, v117
	v_cvt_pk_fp8_f32 v242, v240, v241 op_sel:[0,0,1]
	global_store_dword v[248:249], v242, off offset:-512
	v_mov_b32_e32 v242, 0
	v_mul_f32_e32 v238, v236, v214
	v_mul_f32_e32 v239, v236, v215
	v_mul_f32_e32 v238, v238, v118
	v_mul_f32_e32 v239, v239, v119
	v_cvt_pk_fp8_f32 v242, v238, v239
	v_mul_f32_e32 v240, v236, v216
	v_mul_f32_e32 v241, v236, v217
	v_mul_f32_e32 v240, v240, v120
	v_mul_f32_e32 v241, v241, v121
	v_cvt_pk_fp8_f32 v242, v240, v241 op_sel:[0,0,1]
	global_store_dword v[248:249], v242, off offset:-256
	v_mov_b32_e32 v242, 0
	v_mul_f32_e32 v238, v236, v218
	v_mul_f32_e32 v239, v236, v219
	v_mul_f32_e32 v238, v238, v122
	v_mul_f32_e32 v239, v239, v123
	v_cvt_pk_fp8_f32 v242, v238, v239
	v_mul_f32_e32 v240, v236, v220
	v_mul_f32_e32 v241, v236, v221
	v_mul_f32_e32 v240, v240, v124
	v_mul_f32_e32 v241, v241, v125
	v_cvt_pk_fp8_f32 v242, v240, v241 op_sel:[0,0,1]
	global_store_dword v[248:249], v242, off
	v_mov_b32_e32 v242, 0
	v_mul_f32_e32 v238, v236, v222
	v_mul_f32_e32 v239, v236, v223
	v_mul_f32_e32 v238, v238, v126
	v_mul_f32_e32 v239, v239, v127
	v_cvt_pk_fp8_f32 v242, v238, v239
	v_mul_f32_e32 v240, v236, v224
	v_mul_f32_e32 v241, v236, v225
	v_mul_f32_e32 v240, v240, v128
	v_mul_f32_e32 v241, v241, v129
	v_cvt_pk_fp8_f32 v242, v240, v241 op_sel:[0,0,1]
	global_store_dword v[248:249], v242, off offset:256
	v_mov_b32_e32 v242, 0
	v_mul_f32_e32 v238, v236, v226
	v_mul_f32_e32 v239, v236, v227
	v_mul_f32_e32 v238, v238, v130
	v_mul_f32_e32 v239, v239, v131
	v_cvt_pk_fp8_f32 v242, v238, v239
	v_mul_f32_e32 v240, v236, v228
	v_mul_f32_e32 v241, v236, v229
	v_mul_f32_e32 v240, v240, v132
	v_mul_f32_e32 v241, v241, v133
	v_cvt_pk_fp8_f32 v242, v240, v241 op_sel:[0,0,1]
	global_store_dword v[248:249], v242, off offset:512
	v_mov_b32_e32 v242, 0
	v_mul_f32_e32 v238, v236, v230
	v_mul_f32_e32 v239, v236, v231
	v_mul_f32_e32 v238, v238, v134
	v_mul_f32_e32 v239, v239, v135
	v_cvt_pk_fp8_f32 v242, v238, v239
	v_mul_f32_e32 v240, v236, v232
	v_mul_f32_e32 v241, v236, v233
	v_mul_f32_e32 v240, v240, v136
	v_mul_f32_e32 v241, v241, v137
	v_cvt_pk_fp8_f32 v242, v240, v241 op_sel:[0,0,1]
	global_store_dword v[248:249], v242, off offset:768
	s_waitcnt vmcnt(16)
; __device__ __forceinline__ void phase_router(const Params& p, LAS3 char* lds, int wid) {
;     ...
; #pragma unroll 1
;         for (int q = 0; q < 4; ++q) {
;             const int tk = wid * 4 + q;
;             const float r = rstd[tk];
;             const float* hr = p.h + (size_t)(t0 + tk) * D;
; #pragma unroll
;             for (int j = 0; j < 8; ++j) {
;                 const f32x4 hv = *(const f32x4*)(hr + j * 256 + lane * 4), gg = *(const f32x4*)(p.ln_ffn_g + j * 256 + lane * 4);
;                 int o = __builtin_amdgcn_cvt_pk_fp8_f32(hv[0] * r * gg[0], hv[1] * r * gg[1], 0, false);
;                 o = __builtin_amdgcn_cvt_pk_fp8_f32(hv[2] * r * gg[2], hv[3] * r * gg[3], o, true);
;                 *(int*)((unsigned char*)p.xn2 + (size_t)(t0 + tk) * D + j * 256 + lane * 4) = o;
;             }
;         }
	s_mov_b64 s[26:27], 0x1800
	v_lshl_add_u64 v[248:249], v[2:3], 0, s[26:27]
	v_mov_b32_e32 v242, 0
	v_mul_f32_e32 v238, v237, v138
	v_mul_f32_e32 v239, v237, v139
	v_mul_f32_e32 v238, v238, v106
	v_mul_f32_e32 v239, v239, v107
	v_cvt_pk_fp8_f32 v242, v238, v239
	v_mul_f32_e32 v240, v237, v140
	v_mul_f32_e32 v241, v237, v141
	v_mul_f32_e32 v240, v240, v108
	v_mul_f32_e32 v241, v241, v109
	v_cvt_pk_fp8_f32 v242, v240, v241 op_sel:[0,0,1]
	global_store_dword v[248:249], v242, off offset:-1024
	v_mov_b32_e32 v242, 0
	v_mul_f32_e32 v238, v237, v142
	v_mul_f32_e32 v239, v237, v143
	v_mul_f32_e32 v238, v238, v110
	v_mul_f32_e32 v239, v239, v111
	v_cvt_pk_fp8_f32 v242, v238, v239
	v_mul_f32_e32 v240, v237, v144
	v_mul_f32_e32 v241, v237, v145
	v_mul_f32_e32 v240, v240, v112
	v_mul_f32_e32 v241, v241, v113
	v_cvt_pk_fp8_f32 v242, v240, v241 op_sel:[0,0,1]
	global_store_dword v[248:249], v242, off offset:-768
	v_mov_b32_e32 v242, 0
	v_mul_f32_e32 v238, v237, v146
	v_mul_f32_e32 v239, v237, v147
	v_mul_f32_e32 v238, v238, v114
	v_mul_f32_e32 v239, v239, v115
	v_cvt_pk_fp8_f32 v242, v238, v239
	v_mul_f32_e32 v240, v237, v148
	v_mul_f32_e32 v241, v237, v149
	v_mul_f32_e32 v240, v240, v116
	v_mul_f32_e32 v241, v241, v117
	v_cvt_pk_fp8_f32 v242, v240, v241 op_sel:[0,0,1]
	global_store_dword v[248:249], v242, off offset:-512
	v_mov_b32_e32 v242, 0
	v_mul_f32_e32 v238, v237, v150
	v_mul_f32_e32 v239, v237, v151
	v_mul_f32_e32 v238, v238, v118
	v_mul_f32_e32 v239, v239, v119
	v_cvt_pk_fp8_f32 v242, v238, v239
	v_mul_f32_e32 v240, v237, v152
	v_mul_f32_e32 v241, v237, v153
	v_mul_f32_e32 v240, v240, v120
	v_mul_f32_e32 v241, v241, v121
	v_cvt_pk_fp8_f32 v242, v240, v241 op_sel:[0,0,1]
	global_store_dword v[248:249], v242, off offset:-256
	v_mov_b32_e32 v242, 0
	v_mul_f32_e32 v238, v237, v154
	v_mul_f32_e32 v239, v237, v155
	v_mul_f32_e32 v238, v238, v122
	v_mul_f32_e32 v239, v239, v123
	v_cvt_pk_fp8_f32 v242, v238, v239
	v_mul_f32_e32 v240, v237, v156
	v_mul_f32_e32 v241, v237, v157
	v_mul_f32_e32 v240, v240, v124
	v_mul_f32_e32 v241, v241, v125
	v_cvt_pk_fp8_f32 v242, v240, v241 op_sel:[0,0,1]
	global_store_dword v[248:249], v242, off
	v_mov_b32_e32 v242, 0
	v_mul_f32_e32 v238, v237, v158
	v_mul_f32_e32 v239, v237, v159
	v_mul_f32_e32 v238, v238, v126
	v_mul_f32_e32 v239, v239, v127
	v_cvt_pk_fp8_f32 v242, v238, v239
	v_mul_f32_e32 v240, v237, v160
	v_mul_f32_e32 v241, v237, v161
	v_mul_f32_e32 v240, v240, v128
	v_mul_f32_e32 v241, v241, v129
	v_cvt_pk_fp8_f32 v242, v240, v241 op_sel:[0,0,1]
	global_store_dword v[248:249], v242, off offset:256
	v_mov_b32_e32 v242, 0
	v_mul_f32_e32 v238, v237, v162
	v_mul_f32_e32 v239, v237, v163
	v_mul_f32_e32 v238, v238, v130
	v_mul_f32_e32 v239, v239, v131
	v_cvt_pk_fp8_f32 v242, v238, v239
	v_mul_f32_e32 v240, v237, v164
	v_mul_f32_e32 v241, v237, v165
	v_mul_f32_e32 v240, v240, v132
	v_mul_f32_e32 v241, v241, v133
	v_cvt_pk_fp8_f32 v242, v240, v241 op_sel:[0,0,1]
	global_store_dword v[248:249], v242, off offset:512
	v_mov_b32_e32 v242, 0
	v_mul_f32_e32 v238, v237, v166
	v_mul_f32_e32 v239, v237, v167
	v_mul_f32_e32 v238, v238, v134
	v_mul_f32_e32 v239, v239, v135
	v_cvt_pk_fp8_f32 v242, v238, v239
	v_mul_f32_e32 v240, v237, v168
	v_mul_f32_e32 v241, v237, v169
	v_mul_f32_e32 v240, v240, v136
	v_mul_f32_e32 v241, v241, v137
	v_cvt_pk_fp8_f32 v242, v240, v241 op_sel:[0,0,1]
	global_store_dword v[248:249], v242, off offset:768
	s_add_i32 s21, s21, s80
	s_add_i32 s10, s10, s3
	s_cmpk_gt_i32 s21, 0xff
	v_add_u32_e32 v50, s3, v50
	s_cbranch_scc0 .LBB0_335

; #define LAS3 __attribute__((address_space(3)))
; template <int EPI>
; __device__ __forceinline__ void gemm_tile_img(const GemmArgs& g, int pm, int pn, int e, int ebase, int ecnt, LAS3 char* lds, int wid, const unsigned char* img, const TileSync& sy, int kh = -1) {
;     ...
;         for (int n = 0; n < 2; ++n) { bgate[n] = *(LAS3 const f32x4*)(lds + LDS_BIAS + (n * 64 + colw) * 4); bup1[n] = *(LAS3 const f32x4*)(lds + LDS_BIAS + (128 + n * 64 + colw) * 4); }
; #pragma unroll
;         for (int ai = 0; ai < 2; ++ai)
; #pragma unroll
;             for (int m = 0; m < 4; ++m) {
;                 const int r = pm * 256 + ai * 128 + row0 + m * 16;
;                 {
;                     LAS3 char* rp = lds + (ai * 128 + row0 + m * 16) * EST_F8 + colw;
; #pragma unroll
;                     for (int n = 0; n < 2; ++n) {
;                         float o[4];
; #pragma unroll
;                         for (int j = 0; j < 4; j += 2) {
;                             typedef float f32x2 __attribute__((ext_vector_type(2)));
;                             f32x2 gt = (f32x2){acc[ai][0][m][n][j], acc[ai][0][m][n][j + 1]} + (f32x2){bgate[n][j], bgate[n][j + 1]};
;                             f32x2 up = (f32x2){acc[ai][1][m][n][j], acc[ai][1][m][n][j + 1]} + (f32x2){bup1[n][j], bup1[n][j + 1]};
;                             gt.x = fminf(gt.x, 7.0f); gt.y = fminf(gt.y, 7.0f);
;                             up.x = __builtin_amdgcn_fmed3f(up.x, -6.0f, 8.0f); up.y = __builtin_amdgcn_fmed3f(up.y, -6.0f, 8.0f);
;                             const f32x2 xe = gt * (-2.45546696f);
;                             f32x2 ex; ex.x = __builtin_amdgcn_exp2f(xe.x); ex.y = __builtin_amdgcn_exp2f(xe.y);
;                             const f32x2 den = ex + 1.0f;
;                             f32x2 rc; rc.x = __builtin_amdgcn_rcpf(den.x); rc.y = __builtin_amdgcn_rcpf(den.y);
;                             const f32x2 res = (gt * rc) * up;
;                             o[j] = res.x; o[j + 1] = res.y;
;                         }
;                         int w = __builtin_amdgcn_cvt_pk_fp8_f32(o[0], o[1], 0, false);
;                         w = __builtin_amdgcn_cvt_pk_fp8_f32(o[2], o[3], w, true);
;                         *(LAS3 int*)(rp + n * 64) = w;
.LBB0_477:
	s_or_b64 exec, exec, s[0:1]
	v_lshrrev_b32_e32 v81, 2, v152
	v_and_b32_e32 v82, 60, v81
	v_lshl_add_u32 v0, v82, 2, 0
	v_and_b32_e32 v80, 15, v152
	v_add_u32_e32 v4, 0x21c00, v0
	s_mov_b32 s0, 0xfffffc0
	ds_read_b128 v[12:15], v4
	ds_read_b128 v[8:11], v4 offset:512
	ds_read_b128 v[0:3], v4 offset:256
	ds_read_b128 v[4:7], v4 offset:768
	v_and_or_b32 v80, v81, s0, v80
	v_mul_lo_u32 v80, v80, s25
	v_add3_u32 v153, 0, v82, v80
	s_waitcnt lgkmcnt(3)
	v_pk_add_f32 v[82:83], v[140:141], v[12:13]
	s_mov_b32 s4, 0xc01d265f
	v_min_f32_e32 v82, 0x40e00000, v82
	v_min_f32_e32 v83, 0x40e00000, v83
	v_pk_mul_f32 v[140:141], v[82:83], s[4:5] op_sel_hi:[1,0]
	v_pk_add_f32 v[80:81], v[142:143], v[14:15]
	v_exp_f32_e32 v140, v140
	v_exp_f32_e32 v141, v141
	s_waitcnt lgkmcnt(2)
	v_pk_add_f32 v[136:137], v[136:137], v[8:9]
	s_mov_b32 s0, 0xc0c00000
	v_pk_add_f32 v[138:139], v[138:139], v[10:11]
	v_pk_add_f32 v[140:141], v[140:141], 1.0 op_sel_hi:[1,0]
	v_med3_f32 v136, v136, s0, v146
	v_rcp_f32_e32 v140, v140
	v_rcp_f32_e32 v141, v141
	v_med3_f32 v137, v137, s0, v146
	v_min_f32_e32 v80, 0x40e00000, v80
	v_min_f32_e32 v81, 0x40e00000, v81
	v_pk_mul_f32 v[82:83], v[82:83], v[140:141]
	s_waitcnt lgkmcnt(0)
	v_pk_add_f32 v[128:129], v[128:129], v[4:5]
	v_pk_mul_f32 v[82:83], v[136:137], v[82:83]
	v_med3_f32 v136, v138, s0, v146
	v_med3_f32 v137, v139, s0, v146
	v_pk_mul_f32 v[138:139], v[80:81], s[4:5] op_sel_hi:[1,0]
	v_pk_add_f32 v[130:131], v[130:131], v[6:7]
	v_exp_f32_e32 v138, v138
	v_exp_f32_e32 v139, v139
	v_med3_f32 v128, v128, s0, v146
	v_med3_f32 v129, v129, s0, v146
	v_pk_add_f32 v[120:121], v[120:121], v[8:9]
	v_pk_add_f32 v[138:139], v[138:139], 1.0 op_sel_hi:[1,0]
	v_pk_add_f32 v[122:123], v[122:123], v[10:11]
	v_rcp_f32_e32 v138, v138
	v_rcp_f32_e32 v139, v139
	v_med3_f32 v120, v120, s0, v146
	v_med3_f32 v121, v121, s0, v146
	v_pk_add_f32 v[112:113], v[112:113], v[4:5]
	v_pk_mul_f32 v[80:81], v[80:81], v[138:139]
	v_pk_add_f32 v[114:115], v[114:115], v[6:7]
	v_pk_mul_f32 v[80:81], v[136:137], v[80:81]
	v_mov_b32_e32 v136, 0
	v_cvt_pk_fp8_f32 v136, v82, v83
	v_pk_add_f32 v[82:83], v[132:133], v[0:1]
	v_med3_f32 v112, v112, s0, v146
	v_min_f32_e32 v82, 0x40e00000, v82
	v_min_f32_e32 v83, 0x40e00000, v83
	v_pk_mul_f32 v[132:133], v[82:83], s[4:5] op_sel_hi:[1,0]
	v_cvt_pk_fp8_f32 v136, v80, v81 op_sel:[0,0,1]
	v_exp_f32_e32 v132, v132
	v_exp_f32_e32 v133, v133
	v_pk_add_f32 v[80:81], v[134:135], v[2:3]
	v_med3_f32 v113, v113, s0, v146
	v_min_f32_e32 v80, 0x40e00000, v80
	v_pk_add_f32 v[132:133], v[132:133], 1.0 op_sel_hi:[1,0]
	v_min_f32_e32 v81, 0x40e00000, v81
	v_rcp_f32_e32 v132, v132
	v_rcp_f32_e32 v133, v133
	v_pk_add_f32 v[104:105], v[104:105], v[8:9]
	v_pk_add_f32 v[106:107], v[106:107], v[10:11]
	v_med3_f32 v104, v104, s0, v146
	v_pk_mul_f32 v[82:83], v[82:83], v[132:133]
	v_med3_f32 v105, v105, s0, v146
	v_pk_mul_f32 v[82:83], v[128:129], v[82:83]
	v_med3_f32 v128, v130, s0, v146
	v_med3_f32 v129, v131, s0, v146
	v_pk_mul_f32 v[130:131], v[80:81], s[4:5] op_sel_hi:[1,0]
	v_pk_add_f32 v[96:97], v[96:97], v[4:5]
	v_exp_f32_e32 v130, v130
	v_exp_f32_e32 v131, v131
	v_pk_add_f32 v[98:99], v[98:99], v[6:7]
	v_med3_f32 v96, v96, s0, v146
	v_med3_f32 v97, v97, s0, v146
	v_pk_add_f32 v[130:131], v[130:131], 1.0 op_sel_hi:[1,0]
	v_pk_add_f32 v[88:89], v[88:89], v[8:9]
	v_rcp_f32_e32 v130, v130
	v_rcp_f32_e32 v131, v131
	v_pk_add_f32 v[90:91], v[90:91], v[10:11]
	v_med3_f32 v88, v88, s0, v146
	v_med3_f32 v89, v89, s0, v146
	v_pk_mul_f32 v[80:81], v[80:81], v[130:131]
	v_pk_add_f32 v[20:21], v[20:21], v[4:5]
	v_pk_mul_f32 v[80:81], v[128:129], v[80:81]
	v_mov_b32_e32 v128, 0
	v_cvt_pk_fp8_f32 v128, v82, v83
	v_pk_add_f32 v[82:83], v[124:125], v[12:13]
	v_med3_f32 v20, v20, s0, v146
	v_min_f32_e32 v82, 0x40e00000, v82
	v_min_f32_e32 v83, 0x40e00000, v83
	v_pk_mul_f32 v[124:125], v[82:83], s[4:5] op_sel_hi:[1,0]
	v_cvt_pk_fp8_f32 v128, v80, v81 op_sel:[0,0,1]
	v_exp_f32_e32 v124, v124
	v_exp_f32_e32 v125, v125
	v_pk_add_f32 v[80:81], v[126:127], v[14:15]
	v_med3_f32 v21, v21, s0, v146
	v_min_f32_e32 v80, 0x40e00000, v80
	v_pk_add_f32 v[124:125], v[124:125], 1.0 op_sel_hi:[1,0]
	v_min_f32_e32 v81, 0x40e00000, v81
	v_rcp_f32_e32 v124, v124
	v_rcp_f32_e32 v125, v125
	v_pk_add_f32 v[22:23], v[22:23], v[6:7]
	v_pk_add_f32 v[72:73], v[72:73], v[8:9]
	v_med3_f32 v22, v22, s0, v146
	v_pk_mul_f32 v[82:83], v[82:83], v[124:125]
	v_med3_f32 v23, v23, s0, v146
	v_pk_mul_f32 v[82:83], v[120:121], v[82:83]
	v_med3_f32 v120, v122, s0, v146
	v_med3_f32 v121, v123, s0, v146
	v_pk_mul_f32 v[122:123], v[80:81], s[4:5] op_sel_hi:[1,0]
	v_pk_add_f32 v[74:75], v[74:75], v[10:11]
	v_exp_f32_e32 v122, v122
	v_exp_f32_e32 v123, v123
	v_med3_f32 v72, v72, s0, v146
	v_med3_f32 v73, v73, s0, v146
	v_pk_add_f32 v[64:65], v[64:65], v[4:5]
	v_pk_add_f32 v[122:123], v[122:123], 1.0 op_sel_hi:[1,0]
	v_pk_add_f32 v[66:67], v[66:67], v[6:7]
	v_rcp_f32_e32 v122, v122
	v_rcp_f32_e32 v123, v123
	v_med3_f32 v64, v64, s0, v146
	v_med3_f32 v65, v65, s0, v146
	v_pk_add_f32 v[56:57], v[56:57], v[8:9]
	v_pk_mul_f32 v[80:81], v[80:81], v[122:123]
	v_pk_add_f32 v[58:59], v[58:59], v[10:11]
	v_pk_mul_f32 v[80:81], v[120:121], v[80:81]
	v_mov_b32_e32 v120, 0
	v_cvt_pk_fp8_f32 v120, v82, v83
	v_pk_add_f32 v[82:83], v[116:117], v[0:1]
	v_med3_f32 v56, v56, s0, v146
	v_min_f32_e32 v82, 0x40e00000, v82
	v_min_f32_e32 v83, 0x40e00000, v83
	v_pk_mul_f32 v[116:117], v[82:83], s[4:5] op_sel_hi:[1,0]
	v_cvt_pk_fp8_f32 v120, v80, v81 op_sel:[0,0,1]
	v_exp_f32_e32 v116, v116
	v_exp_f32_e32 v117, v117
	v_pk_add_f32 v[80:81], v[118:119], v[2:3]
	v_med3_f32 v57, v57, s0, v146
	v_min_f32_e32 v80, 0x40e00000, v80
; #define LAS3 __attribute__((address_space(3)))
; template <int EPI>
; __device__ __forceinline__ void gemm_tile_img(const GemmArgs& g, int pm, int pn, int e, int ebase, int ecnt, LAS3 char* lds, int wid, const unsigned char* img, const TileSync& sy, int kh = -1) {
;     ...
;                         for (int j = 0; j < 4; j += 2) {
;                             typedef float f32x2 __attribute__((ext_vector_type(2)));
;                             f32x2 gt = (f32x2){acc[ai][0][m][n][j], acc[ai][0][m][n][j + 1]} + (f32x2){bgate[n][j], bgate[n][j + 1]};
;                             f32x2 up = (f32x2){acc[ai][1][m][n][j], acc[ai][1][m][n][j + 1]} + (f32x2){bup1[n][j], bup1[n][j + 1]};
;                             gt.x = fminf(gt.x, 7.0f); gt.y = fminf(gt.y, 7.0f);
;                             up.x = __builtin_amdgcn_fmed3f(up.x, -6.0f, 8.0f); up.y = __builtin_amdgcn_fmed3f(up.y, -6.0f, 8.0f);
;                             const f32x2 xe = gt * (-2.45546696f);
;                             f32x2 ex; ex.x = __builtin_amdgcn_exp2f(xe.x); ex.y = __builtin_amdgcn_exp2f(xe.y);
;                             const f32x2 den = ex + 1.0f;
;                             f32x2 rc; rc.x = __builtin_amdgcn_rcpf(den.x); rc.y = __builtin_amdgcn_rcpf(den.y);
;                             const f32x2 res = (gt * rc) * up;
;                             o[j] = res.x; o[j + 1] = res.y;
;                         }
;                         int w = __builtin_amdgcn_cvt_pk_fp8_f32(o[0], o[1], 0, false);
;                         w = __builtin_amdgcn_cvt_pk_fp8_f32(o[2], o[3], w, true);
;                         *(LAS3 int*)(rp + n * 64) = w;
	v_pk_add_f32 v[116:117], v[116:117], 1.0 op_sel_hi:[1,0]
	v_min_f32_e32 v81, 0x40e00000, v81
	v_rcp_f32_e32 v116, v116
	v_rcp_f32_e32 v117, v117
	v_pk_add_f32 v[48:49], v[48:49], v[4:5]
	v_pk_add_f32 v[50:51], v[50:51], v[6:7]
	v_med3_f32 v48, v48, s0, v146
	v_pk_mul_f32 v[82:83], v[82:83], v[116:117]
	v_med3_f32 v49, v49, s0, v146
	v_pk_mul_f32 v[82:83], v[112:113], v[82:83]
	v_med3_f32 v112, v114, s0, v146
	v_med3_f32 v113, v115, s0, v146
	v_pk_mul_f32 v[114:115], v[80:81], s[4:5] op_sel_hi:[1,0]
	v_pk_add_f32 v[40:41], v[40:41], v[8:9]
	v_exp_f32_e32 v114, v114
	v_exp_f32_e32 v115, v115
	v_pk_add_f32 v[42:43], v[42:43], v[10:11]
	v_med3_f32 v40, v40, s0, v146
	v_med3_f32 v41, v41, s0, v146
	v_pk_add_f32 v[114:115], v[114:115], 1.0 op_sel_hi:[1,0]
	v_pk_add_f32 v[32:33], v[32:33], v[4:5]
	v_rcp_f32_e32 v114, v114
	v_rcp_f32_e32 v115, v115
	v_pk_add_f32 v[34:35], v[34:35], v[6:7]
	v_med3_f32 v32, v32, s0, v146
	v_med3_f32 v33, v33, s0, v146
	v_pk_mul_f32 v[80:81], v[80:81], v[114:115]
	v_pk_add_f32 v[8:9], v[24:25], v[8:9]
	v_pk_mul_f32 v[80:81], v[112:113], v[80:81]
	v_mov_b32_e32 v112, 0
	v_cvt_pk_fp8_f32 v112, v82, v83
	v_pk_add_f32 v[82:83], v[108:109], v[12:13]
	v_med3_f32 v8, v8, s0, v146
	v_min_f32_e32 v82, 0x40e00000, v82
	v_min_f32_e32 v83, 0x40e00000, v83
	v_pk_mul_f32 v[108:109], v[82:83], s[4:5] op_sel_hi:[1,0]
	v_cvt_pk_fp8_f32 v112, v80, v81 op_sel:[0,0,1]
	v_exp_f32_e32 v108, v108
	v_exp_f32_e32 v109, v109
	v_add_u32_e32 v80, 0x800, v153
	ds_write2_b32 v80, v120, v112 offset0:64 offset1:80
	v_pk_add_f32 v[80:81], v[110:111], v[14:15]
	v_pk_add_f32 v[108:109], v[108:109], 1.0 op_sel_hi:[1,0]
	v_min_f32_e32 v80, 0x40e00000, v80
	v_rcp_f32_e32 v108, v108
	v_rcp_f32_e32 v109, v109
	v_min_f32_e32 v81, 0x40e00000, v81
	v_med3_f32 v9, v9, s0, v146
	v_pk_add_f32 v[10:11], v[26:27], v[10:11]
	v_pk_mul_f32 v[82:83], v[82:83], v[108:109]
	v_med3_f32 v10, v10, s0, v146
	v_pk_mul_f32 v[82:83], v[104:105], v[82:83]
	v_med3_f32 v104, v106, s0, v146
	v_med3_f32 v105, v107, s0, v146
	v_pk_mul_f32 v[106:107], v[80:81], s[4:5] op_sel_hi:[1,0]
	v_med3_f32 v11, v11, s0, v146
	v_exp_f32_e32 v106, v106
	v_exp_f32_e32 v107, v107
	v_pk_add_f32 v[4:5], v[16:17], v[4:5]
	v_pk_add_f32 v[6:7], v[18:19], v[6:7]
	v_med3_f32 v4, v4, s0, v146
	v_pk_add_f32 v[106:107], v[106:107], 1.0 op_sel_hi:[1,0]
	v_med3_f32 v5, v5, s0, v146
	v_rcp_f32_e32 v106, v106
	v_rcp_f32_e32 v107, v107
	v_readlane_b32 s1, v255, 12
	ds_write2_b32 v153, v136, v128 offset1:16
	v_pk_mul_f32 v[80:81], v[80:81], v[106:107]
	s_nop 0
	v_pk_mul_f32 v[80:81], v[104:105], v[80:81]
	v_mov_b32_e32 v104, 0
	v_cvt_pk_fp8_f32 v104, v82, v83
	v_pk_add_f32 v[82:83], v[100:101], v[0:1]
	v_cvt_pk_fp8_f32 v104, v80, v81 op_sel:[0,0,1]
	v_min_f32_e32 v82, 0x40e00000, v82
	v_min_f32_e32 v83, 0x40e00000, v83
	v_pk_mul_f32 v[100:101], v[82:83], s[4:5] op_sel_hi:[1,0]
	v_pk_add_f32 v[80:81], v[102:103], v[2:3]
	v_exp_f32_e32 v100, v100
	v_exp_f32_e32 v101, v101
	v_min_f32_e32 v80, 0x40e00000, v80
	v_min_f32_e32 v81, 0x40e00000, v81
	v_pk_add_f32 v[100:101], v[100:101], 1.0 op_sel_hi:[1,0]
	s_nop 0
	v_rcp_f32_e32 v100, v100
	v_rcp_f32_e32 v101, v101
	s_nop 0
	v_pk_mul_f32 v[82:83], v[82:83], v[100:101]
	s_nop 0
	v_pk_mul_f32 v[82:83], v[96:97], v[82:83]
	v_med3_f32 v96, v98, s0, v146
	v_med3_f32 v97, v99, s0, v146
	v_pk_mul_f32 v[98:99], v[80:81], s[4:5] op_sel_hi:[1,0]
	s_nop 0
	v_exp_f32_e32 v98, v98
	v_exp_f32_e32 v99, v99
	s_nop 0
	v_pk_add_f32 v[98:99], v[98:99], 1.0 op_sel_hi:[1,0]
	s_nop 0
	v_rcp_f32_e32 v98, v98
	v_rcp_f32_e32 v99, v99
	s_nop 0
	v_pk_mul_f32 v[80:81], v[80:81], v[98:99]
	s_nop 0
	v_pk_mul_f32 v[80:81], v[96:97], v[80:81]
	v_mov_b32_e32 v96, 0
	v_cvt_pk_fp8_f32 v96, v82, v83
	v_pk_add_f32 v[82:83], v[92:93], v[12:13]
	v_cvt_pk_fp8_f32 v96, v80, v81 op_sel:[0,0,1]
	v_min_f32_e32 v82, 0x40e00000, v82
	v_min_f32_e32 v83, 0x40e00000, v83
	v_pk_mul_f32 v[92:93], v[82:83], s[4:5] op_sel_hi:[1,0]
	v_add_u32_e32 v80, 0x1000, v153
	v_exp_f32_e32 v92, v92
	v_exp_f32_e32 v93, v93
	ds_write2_b32 v80, v104, v96 offset0:128 offset1:144
	v_pk_add_f32 v[80:81], v[94:95], v[14:15]
	v_pk_add_f32 v[92:93], v[92:93], 1.0 op_sel_hi:[1,0]
	s_nop 0
	v_rcp_f32_e32 v92, v92
	v_rcp_f32_e32 v93, v93
	v_min_f32_e32 v80, 0x40e00000, v80
	v_min_f32_e32 v81, 0x40e00000, v81
	v_pk_mul_f32 v[82:83], v[82:83], v[92:93]
	s_nop 0
	v_pk_mul_f32 v[82:83], v[88:89], v[82:83]
	v_med3_f32 v88, v90, s0, v146
	v_med3_f32 v89, v91, s0, v146
	v_pk_mul_f32 v[90:91], v[80:81], s[4:5] op_sel_hi:[1,0]
	s_nop 0
	v_exp_f32_e32 v90, v90
	v_exp_f32_e32 v91, v91
	s_nop 0
	v_pk_add_f32 v[90:91], v[90:91], 1.0 op_sel_hi:[1,0]
	s_nop 0
	v_rcp_f32_e32 v90, v90
	v_rcp_f32_e32 v91, v91
	s_nop 0
	v_pk_mul_f32 v[80:81], v[80:81], v[90:91]
	s_nop 0
	v_pk_mul_f32 v[80:81], v[88:89], v[80:81]
	v_mov_b32_e32 v88, 0
	v_cvt_pk_fp8_f32 v88, v82, v83
	v_pk_add_f32 v[82:83], v[84:85], v[0:1]
	v_cvt_pk_fp8_f32 v88, v80, v81 op_sel:[0,0,1]
	v_min_f32_e32 v82, 0x40e00000, v82
	v_min_f32_e32 v83, 0x40e00000, v83
	v_pk_mul_f32 v[84:85], v[82:83], s[4:5] op_sel_hi:[1,0]
	v_pk_add_f32 v[80:81], v[86:87], v[2:3]
	v_exp_f32_e32 v84, v84
	v_exp_f32_e32 v85, v85
	v_min_f32_e32 v80, 0x40e00000, v80
	v_min_f32_e32 v81, 0x40e00000, v81
	v_pk_add_f32 v[84:85], v[84:85], 1.0 op_sel_hi:[1,0]
	s_nop 0
	v_rcp_f32_e32 v84, v84
	v_rcp_f32_e32 v85, v85
	s_nop 0
	v_pk_mul_f32 v[82:83], v[82:83], v[84:85]
	s_nop 0
	v_pk_mul_f32 v[20:21], v[20:21], v[82:83]
	v_pk_mul_f32 v[82:83], v[80:81], s[4:5] op_sel_hi:[1,0]
	s_nop 0
	v_exp_f32_e32 v82, v82
	v_exp_f32_e32 v83, v83
	s_nop 0
	v_pk_add_f32 v[82:83], v[82:83], 1.0 op_sel_hi:[1,0]
	s_nop 0
	v_rcp_f32_e32 v82, v82
; #define LAS3 __attribute__((address_space(3)))
; template <int EPI>
; __device__ __forceinline__ void gemm_tile_img(const GemmArgs& g, int pm, int pn, int e, int ebase, int ecnt, LAS3 char* lds, int wid, const unsigned char* img, const TileSync& sy, int kh = -1) {
;     ...
;                         for (int j = 0; j < 4; j += 2) {
;                             typedef float f32x2 __attribute__((ext_vector_type(2)));
;                             f32x2 gt = (f32x2){acc[ai][0][m][n][j], acc[ai][0][m][n][j + 1]} + (f32x2){bgate[n][j], bgate[n][j + 1]};
;                             f32x2 up = (f32x2){acc[ai][1][m][n][j], acc[ai][1][m][n][j + 1]} + (f32x2){bup1[n][j], bup1[n][j + 1]};
;                             gt.x = fminf(gt.x, 7.0f); gt.y = fminf(gt.y, 7.0f);
;                             up.x = __builtin_amdgcn_fmed3f(up.x, -6.0f, 8.0f); up.y = __builtin_amdgcn_fmed3f(up.y, -6.0f, 8.0f);
;                             const f32x2 xe = gt * (-2.45546696f);
;                             f32x2 ex; ex.x = __builtin_amdgcn_exp2f(xe.x); ex.y = __builtin_amdgcn_exp2f(xe.y);
;                             const f32x2 den = ex + 1.0f;
;                             f32x2 rc; rc.x = __builtin_amdgcn_rcpf(den.x); rc.y = __builtin_amdgcn_rcpf(den.y);
;                             const f32x2 res = (gt * rc) * up;
;                             o[j] = res.x; o[j + 1] = res.y;
;                         }
;                         int w = __builtin_amdgcn_cvt_pk_fp8_f32(o[0], o[1], 0, false);
;                         w = __builtin_amdgcn_cvt_pk_fp8_f32(o[2], o[3], w, true);
;                         *(LAS3 int*)(rp + n * 64) = w;
	v_rcp_f32_e32 v83, v83
	s_nop 0
	v_pk_mul_f32 v[80:81], v[80:81], v[82:83]
	s_nop 0
	v_pk_mul_f32 v[22:23], v[22:23], v[80:81]
	v_mov_b32_e32 v80, 0
	v_cvt_pk_fp8_f32 v80, v20, v21
	v_add_u32_e32 v20, 0x1800, v153
	v_cvt_pk_fp8_f32 v80, v22, v23 op_sel:[0,0,1]
	v_pk_add_f32 v[22:23], v[76:77], v[12:13]
	ds_write2_b32 v20, v88, v80 offset0:192 offset1:208
	v_min_f32_e32 v22, 0x40e00000, v22
	v_min_f32_e32 v23, 0x40e00000, v23
	v_pk_mul_f32 v[76:77], v[22:23], s[4:5] op_sel_hi:[1,0]
	v_pk_add_f32 v[20:21], v[78:79], v[14:15]
	v_exp_f32_e32 v76, v76
	v_exp_f32_e32 v77, v77
	v_min_f32_e32 v20, 0x40e00000, v20
	v_min_f32_e32 v21, 0x40e00000, v21
	v_pk_add_f32 v[76:77], v[76:77], 1.0 op_sel_hi:[1,0]
	s_nop 0
	v_rcp_f32_e32 v76, v76
	v_rcp_f32_e32 v77, v77
	s_nop 0
	v_pk_mul_f32 v[22:23], v[22:23], v[76:77]
	s_nop 0
	v_pk_mul_f32 v[22:23], v[72:73], v[22:23]
	v_med3_f32 v72, v74, s0, v146
	v_med3_f32 v73, v75, s0, v146
	v_pk_mul_f32 v[74:75], v[20:21], s[4:5] op_sel_hi:[1,0]
	s_nop 0
	v_exp_f32_e32 v74, v74
	v_exp_f32_e32 v75, v75
	s_nop 0
	v_pk_add_f32 v[74:75], v[74:75], 1.0 op_sel_hi:[1,0]
	s_nop 0
	v_rcp_f32_e32 v74, v74
	v_rcp_f32_e32 v75, v75
	s_nop 0
	v_pk_mul_f32 v[20:21], v[20:21], v[74:75]
	s_nop 0
	v_pk_mul_f32 v[20:21], v[72:73], v[20:21]
	v_mov_b32_e32 v72, 0
	v_cvt_pk_fp8_f32 v72, v22, v23
	v_pk_add_f32 v[22:23], v[68:69], v[0:1]
	v_cvt_pk_fp8_f32 v72, v20, v21 op_sel:[0,0,1]
	v_min_f32_e32 v22, 0x40e00000, v22
	v_min_f32_e32 v23, 0x40e00000, v23
	v_pk_mul_f32 v[68:69], v[22:23], s[4:5] op_sel_hi:[1,0]
	v_pk_add_f32 v[20:21], v[70:71], v[2:3]
	v_exp_f32_e32 v68, v68
	v_exp_f32_e32 v69, v69
	v_min_f32_e32 v20, 0x40e00000, v20
	v_min_f32_e32 v21, 0x40e00000, v21
	v_pk_add_f32 v[68:69], v[68:69], 1.0 op_sel_hi:[1,0]
	s_nop 0
	v_rcp_f32_e32 v68, v68
	v_rcp_f32_e32 v69, v69
	s_nop 0
	v_pk_mul_f32 v[22:23], v[22:23], v[68:69]
	s_nop 0
	v_pk_mul_f32 v[22:23], v[64:65], v[22:23]
	v_med3_f32 v64, v66, s0, v146
	v_med3_f32 v65, v67, s0, v146
	v_pk_mul_f32 v[66:67], v[20:21], s[4:5] op_sel_hi:[1,0]
	s_nop 0
	v_exp_f32_e32 v66, v66
	v_exp_f32_e32 v67, v67
	s_nop 0
	v_pk_add_f32 v[66:67], v[66:67], 1.0 op_sel_hi:[1,0]
	s_nop 0
	v_rcp_f32_e32 v66, v66
	v_rcp_f32_e32 v67, v67
	s_nop 0
	v_pk_mul_f32 v[20:21], v[20:21], v[66:67]
	s_nop 0
	v_pk_mul_f32 v[20:21], v[64:65], v[20:21]
	v_mov_b32_e32 v64, 0
	v_cvt_pk_fp8_f32 v64, v22, v23
	v_pk_add_f32 v[22:23], v[60:61], v[12:13]
	v_cvt_pk_fp8_f32 v64, v20, v21 op_sel:[0,0,1]
	v_min_f32_e32 v22, 0x40e00000, v22
	v_min_f32_e32 v23, 0x40e00000, v23
	v_pk_mul_f32 v[60:61], v[22:23], s[4:5] op_sel_hi:[1,0]
	v_add_u32_e32 v20, 0x4800, v153
	v_exp_f32_e32 v60, v60
	v_exp_f32_e32 v61, v61
	ds_write2_b32 v20, v72, v64 offset1:16
	v_pk_add_f32 v[20:21], v[62:63], v[14:15]
	v_pk_add_f32 v[60:61], v[60:61], 1.0 op_sel_hi:[1,0]
	s_nop 0
	v_rcp_f32_e32 v60, v60
	v_rcp_f32_e32 v61, v61
	v_min_f32_e32 v20, 0x40e00000, v20
	v_min_f32_e32 v21, 0x40e00000, v21
	v_pk_mul_f32 v[22:23], v[22:23], v[60:61]
	s_nop 0
	v_pk_mul_f32 v[22:23], v[56:57], v[22:23]
	v_med3_f32 v56, v58, s0, v146
	v_med3_f32 v57, v59, s0, v146
	v_pk_mul_f32 v[58:59], v[20:21], s[4:5] op_sel_hi:[1,0]
	s_nop 0
	v_exp_f32_e32 v58, v58
	v_exp_f32_e32 v59, v59
	s_nop 0
	v_pk_add_f32 v[58:59], v[58:59], 1.0 op_sel_hi:[1,0]
	s_nop 0
	v_rcp_f32_e32 v58, v58
	v_rcp_f32_e32 v59, v59
	s_nop 0
	v_pk_mul_f32 v[20:21], v[20:21], v[58:59]
	s_nop 0
	v_pk_mul_f32 v[20:21], v[56:57], v[20:21]
	v_mov_b32_e32 v56, 0
	v_cvt_pk_fp8_f32 v56, v22, v23
	v_pk_add_f32 v[22:23], v[52:53], v[0:1]
	v_cvt_pk_fp8_f32 v56, v20, v21 op_sel:[0,0,1]
	v_min_f32_e32 v22, 0x40e00000, v22
	v_min_f32_e32 v23, 0x40e00000, v23
	v_pk_mul_f32 v[52:53], v[22:23], s[4:5] op_sel_hi:[1,0]
	v_pk_add_f32 v[20:21], v[54:55], v[2:3]
	v_exp_f32_e32 v52, v52
	v_exp_f32_e32 v53, v53
	v_min_f32_e32 v20, 0x40e00000, v20
	v_min_f32_e32 v21, 0x40e00000, v21
	v_pk_add_f32 v[52:53], v[52:53], 1.0 op_sel_hi:[1,0]
	s_nop 0
	v_rcp_f32_e32 v52, v52
	v_rcp_f32_e32 v53, v53
	s_nop 0
	v_pk_mul_f32 v[22:23], v[22:23], v[52:53]
	s_nop 0
	v_pk_mul_f32 v[22:23], v[48:49], v[22:23]
	v_med3_f32 v48, v50, s0, v146
	v_med3_f32 v49, v51, s0, v146
	v_pk_mul_f32 v[50:51], v[20:21], s[4:5] op_sel_hi:[1,0]
	s_nop 0
	v_exp_f32_e32 v50, v50
	v_exp_f32_e32 v51, v51
	s_nop 0
	v_pk_add_f32 v[50:51], v[50:51], 1.0 op_sel_hi:[1,0]
	s_nop 0
	v_rcp_f32_e32 v50, v50
	v_rcp_f32_e32 v51, v51
	s_nop 0
	v_pk_mul_f32 v[20:21], v[20:21], v[50:51]
	s_nop 0
	v_pk_mul_f32 v[20:21], v[48:49], v[20:21]
	v_mov_b32_e32 v48, 0
	v_cvt_pk_fp8_f32 v48, v22, v23
	v_pk_add_f32 v[22:23], v[44:45], v[12:13]
	v_pk_add_f32 v[12:13], v[28:29], v[12:13]
	v_min_f32_e32 v22, 0x40e00000, v22
	v_min_f32_e32 v23, 0x40e00000, v23
	v_pk_mul_f32 v[44:45], v[22:23], s[4:5] op_sel_hi:[1,0]
	v_cvt_pk_fp8_f32 v48, v20, v21 op_sel:[0,0,1]
	v_exp_f32_e32 v44, v44
	v_exp_f32_e32 v45, v45
	v_add_u32_e32 v20, 0x5000, v153
	ds_write2_b32 v20, v56, v48 offset0:64 offset1:80
; #define LAS3 __attribute__((address_space(3)))
; #define LD_WAIT(r) asm volatile("s_waitcnt vmcnt(0)" : "+v"(r) :: "memory")
; template <int EPI>
; __device__ __forceinline__ void gemm_tile_img(const GemmArgs& g, int pm, int pn, int e, int ebase, int ecnt, LAS3 char* lds, int wid, const unsigned char* img, const TileSync& sy, int kh = -1) {
;     ...
;                         for (int j = 0; j < 4; j += 2) {
;                             typedef float f32x2 __attribute__((ext_vector_type(2)));
;                             f32x2 gt = (f32x2){acc[ai][0][m][n][j], acc[ai][0][m][n][j + 1]} + (f32x2){bgate[n][j], bgate[n][j + 1]};
;                             f32x2 up = (f32x2){acc[ai][1][m][n][j], acc[ai][1][m][n][j + 1]} + (f32x2){bup1[n][j], bup1[n][j + 1]};
;                             gt.x = fminf(gt.x, 7.0f); gt.y = fminf(gt.y, 7.0f);
;                             up.x = __builtin_amdgcn_fmed3f(up.x, -6.0f, 8.0f); up.y = __builtin_amdgcn_fmed3f(up.y, -6.0f, 8.0f);
;                             const f32x2 xe = gt * (-2.45546696f);
;                             f32x2 ex; ex.x = __builtin_amdgcn_exp2f(xe.x); ex.y = __builtin_amdgcn_exp2f(xe.y);
;                             const f32x2 den = ex + 1.0f;
;                             f32x2 rc; rc.x = __builtin_amdgcn_rcpf(den.x); rc.y = __builtin_amdgcn_rcpf(den.y);
;                             const f32x2 res = (gt * rc) * up;
;                             o[j] = res.x; o[j + 1] = res.y;
;                         }
;                         int w = __builtin_amdgcn_cvt_pk_fp8_f32(o[0], o[1], 0, false);
;                         w = __builtin_amdgcn_cvt_pk_fp8_f32(o[2], o[3], w, true);
;                         *(LAS3 int*)(rp + n * 64) = w;
;                     }
;                 }
;             }
;         { const int nv = ecnt - pm * 256; epi_flush_f8(C, DFF, g.abase + pm * 256, pn * 128, nv < 256 ? nv : 256, lds, tz); }
;     ...
;     if (EPI >= 2 && tz == 0) { LD_WAIT(nx); *sy.qslot = sy.qtag | nx; }
	v_pk_add_f32 v[20:21], v[46:47], v[14:15]
	v_pk_add_f32 v[44:45], v[44:45], 1.0 op_sel_hi:[1,0]
	v_min_f32_e32 v20, 0x40e00000, v20
	v_rcp_f32_e32 v44, v44
	v_rcp_f32_e32 v45, v45
	v_min_f32_e32 v21, 0x40e00000, v21
	v_min_f32_e32 v12, 0x40e00000, v12
	v_min_f32_e32 v13, 0x40e00000, v13
	v_pk_mul_f32 v[22:23], v[22:23], v[44:45]
	v_pk_add_f32 v[14:15], v[30:31], v[14:15]
	v_pk_mul_f32 v[22:23], v[40:41], v[22:23]
	v_med3_f32 v40, v42, s0, v146
	v_med3_f32 v41, v43, s0, v146
	v_pk_mul_f32 v[42:43], v[20:21], s[4:5] op_sel_hi:[1,0]
	s_nop 0
	v_exp_f32_e32 v42, v42
	v_exp_f32_e32 v43, v43
	s_nop 0
	v_pk_add_f32 v[42:43], v[42:43], 1.0 op_sel_hi:[1,0]
	s_nop 0
	v_rcp_f32_e32 v42, v42
	v_rcp_f32_e32 v43, v43
	s_nop 0
	v_pk_mul_f32 v[20:21], v[20:21], v[42:43]
	s_nop 0
	v_pk_mul_f32 v[20:21], v[40:41], v[20:21]
	v_mov_b32_e32 v40, 0
	v_cvt_pk_fp8_f32 v40, v22, v23
	v_pk_add_f32 v[22:23], v[36:37], v[0:1]
	v_pk_add_f32 v[0:1], v[240:241], v[0:1]
	v_min_f32_e32 v22, 0x40e00000, v22
	v_min_f32_e32 v23, 0x40e00000, v23
	v_pk_mul_f32 v[36:37], v[22:23], s[4:5] op_sel_hi:[1,0]
	v_cvt_pk_fp8_f32 v40, v20, v21 op_sel:[0,0,1]
	v_exp_f32_e32 v36, v36
	v_exp_f32_e32 v37, v37
	v_pk_add_f32 v[20:21], v[38:39], v[2:3]
	v_min_f32_e32 v0, 0x40e00000, v0
	v_min_f32_e32 v20, 0x40e00000, v20
	v_pk_add_f32 v[36:37], v[36:37], 1.0 op_sel_hi:[1,0]
	v_min_f32_e32 v21, 0x40e00000, v21
	v_rcp_f32_e32 v36, v36
	v_rcp_f32_e32 v37, v37
	v_min_f32_e32 v1, 0x40e00000, v1
	v_pk_add_f32 v[2:3], v[242:243], v[2:3]
	v_pk_mul_f32 v[22:23], v[22:23], v[36:37]
	s_nop 0
	v_pk_mul_f32 v[22:23], v[32:33], v[22:23]
	v_med3_f32 v32, v34, s0, v146
	v_med3_f32 v33, v35, s0, v146
	v_pk_mul_f32 v[34:35], v[20:21], s[4:5] op_sel_hi:[1,0]
	v_min_f32_e32 v2, 0x40e00000, v2
	v_exp_f32_e32 v34, v34
	v_exp_f32_e32 v35, v35
	v_min_f32_e32 v3, 0x40e00000, v3
	v_pk_add_f32 v[34:35], v[34:35], 1.0 op_sel_hi:[1,0]
	s_nop 0
	v_rcp_f32_e32 v34, v34
	v_rcp_f32_e32 v35, v35
	s_nop 0
	v_pk_mul_f32 v[20:21], v[20:21], v[34:35]
	s_nop 0
	v_pk_mul_f32 v[20:21], v[32:33], v[20:21]
	v_mov_b32_e32 v32, 0
	v_cvt_pk_fp8_f32 v32, v22, v23
	v_cvt_pk_fp8_f32 v32, v20, v21 op_sel:[0,0,1]
	v_add_u32_e32 v20, 0x5800, v153
	ds_write2_b32 v20, v40, v32 offset0:128 offset1:144
	v_pk_mul_f32 v[20:21], v[12:13], s[4:5] op_sel_hi:[1,0]
	s_nop 0
	v_exp_f32_e32 v20, v20
	v_exp_f32_e32 v21, v21
	s_nop 0
	v_pk_add_f32 v[20:21], v[20:21], 1.0 op_sel_hi:[1,0]
	s_nop 0
	v_rcp_f32_e32 v20, v20
	v_rcp_f32_e32 v21, v21
	s_nop 0
	v_pk_mul_f32 v[12:13], v[12:13], v[20:21]
	s_nop 0
	v_pk_mul_f32 v[8:9], v[8:9], v[12:13]
	v_min_f32_e32 v12, 0x40e00000, v14
	v_min_f32_e32 v13, 0x40e00000, v15
	v_pk_mul_f32 v[14:15], v[12:13], s[4:5] op_sel_hi:[1,0]
	s_nop 0
	v_exp_f32_e32 v14, v14
	v_exp_f32_e32 v15, v15
	s_nop 0
	v_pk_add_f32 v[14:15], v[14:15], 1.0 op_sel_hi:[1,0]
	s_nop 0
	v_rcp_f32_e32 v14, v14
	v_rcp_f32_e32 v15, v15
	s_nop 0
	v_pk_mul_f32 v[12:13], v[12:13], v[14:15]
	s_nop 0
	v_pk_mul_f32 v[10:11], v[10:11], v[12:13]
	v_mov_b32_e32 v12, 0
	v_cvt_pk_fp8_f32 v12, v8, v9
	v_pk_mul_f32 v[8:9], v[0:1], s[4:5] op_sel_hi:[1,0]
	v_cvt_pk_fp8_f32 v12, v10, v11 op_sel:[0,0,1]
	v_exp_f32_e32 v8, v8
	v_exp_f32_e32 v9, v9
	s_nop 0
	v_pk_add_f32 v[8:9], v[8:9], 1.0 op_sel_hi:[1,0]
	s_nop 0
	v_rcp_f32_e32 v8, v8
	v_rcp_f32_e32 v9, v9
	s_nop 0
	v_pk_mul_f32 v[0:1], v[0:1], v[8:9]
	s_nop 0
	v_pk_mul_f32 v[0:1], v[4:5], v[0:1]
	v_med3_f32 v4, v6, s0, v146
	v_med3_f32 v5, v7, s0, v146
	v_pk_mul_f32 v[6:7], v[2:3], s[4:5] op_sel_hi:[1,0]
	v_readlane_b32 s4, v255, 23
	v_exp_f32_e32 v6, v6
	v_exp_f32_e32 v7, v7
	s_sub_i32 s0, s27, s4
	s_add_i32 s1, s1, s4
	s_min_i32 s4, s0, 0x100
	v_pk_add_f32 v[6:7], v[6:7], 1.0 op_sel_hi:[1,0]
	s_lshr_b32 s0, s1, 4
	v_rcp_f32_e32 v6, v6
	v_rcp_f32_e32 v7, v7
	s_and_b32 s0, s0, 0x1fff0
	s_or_b32 s0, s0, s24
	v_pk_mul_f32 v[2:3], v[2:3], v[6:7]
	s_nop 0
	v_pk_mul_f32 v[2:3], v[4:5], v[2:3]
	v_mov_b32_e32 v4, 0
	v_cvt_pk_fp8_f32 v4, v0, v1
	v_add_u32_e32 v0, 0x6000, v153
	v_cvt_pk_fp8_f32 v4, v2, v3 op_sel:[0,0,1]
	v_ashrrev_i32_e32 v2, 3, v152
	ds_write2_b32 v0, v12, v4 offset0:192 offset1:208
	v_lshlrev_b32_e32 v0, 4, v152
	v_and_b32_e32 v1, 0x70, v0
	v_add_u32_e32 v0, 0, v1
	v_lshl_or_b32 v1, s0, 15, v1
	s_waitcnt lgkmcnt(0)
	s_barrier
	s_and_saveexec_b64 s[0:1], vcc
	s_cbranch_execz .Ltk_gu
	v_readlane_b32 s28, v255, 19
	s_waitcnt vmcnt(0)
	s_nop 1
	v_or_b32_e32 v8, s28, v151
	v_readlane_b32 s28, v255, 21
	s_nop 1
	v_mov_b32_e32 v9, s28
	ds_write_b32 v9, v8
.Ltk_gu:
	s_or_b64 exec, exec, s[0:1]
	v_cmp_gt_i32_e64 s[0:1], s4, v2
	s_mov_b64 s[28:29], exec
	s_and_b64 s[0:1], s[28:29], s[0:1]
	s_mov_b64 s[56:57], s[40:41]
	v_mov_b32_e32 v150, 0
	s_mov_b64 exec, s[0:1]
	s_cbranch_execz .LBB0_479
	v_mad_u64_u32 v[4:5], s[0:1], v2, s25, v[0:1]
	v_lshl_add_u32 v3, v2, 7, v1
	ds_read_b128 v[4:7], v4
	s_waitcnt lgkmcnt(0)
	s_nop 4
	global_store_dwordx4 v3, v[4:7], s[64:65] sc1 nt
	s_nop 1

; #define LD_WAIT(r) asm volatile("s_waitcnt vmcnt(0)" : "+v"(r) :: "memory")
; __device__ __forceinline__ void epi_flush_f8(unsigned char* C, size_t ld, int grow0, int col0, int nvalid, LAS3 char* lds, int tid) {
;     ...
;     __syncthreads();
; }
; template <int EPI>
; __device__ __forceinline__ void gemm_tile_img(const GemmArgs& g, int pm, int pn, int e, int ebase, int ecnt, LAS3 char* lds, int wid, const unsigned char* img, const TileSync& sy, int kh = -1) {
;     ...
;     if (EPI >= 2 && tz == 0) { LD_WAIT(nx); *sy.qslot = sy.qtag | nx; }
.LBB0_485:
	s_or_b64 exec, exec, s[28:29]
	s_barrier
	s_and_saveexec_b64 s[0:1], vcc
	s_cbranch_execz .LBB0_487
.LBB0_487:
	s_or_b64 exec, exec, s[0:1]
	v_readlane_b32 s36, v254, 20
	s_lshl_b32 s0, s26, 7
	v_readlane_b32 s50, v254, 34
	s_add_u32 s4, s50, s0
	v_readlane_b32 s0, v255, 13
	v_readlane_b32 s51, v254, 35
	v_readlane_b32 s1, v255, 14
	s_addc_u32 s25, s51, 0
	s_ashr_i32 s1, s0, 31
	s_lshl_b64 s[0:1], s[0:1], 2
	s_add_u32 s0, s4, s0
	s_addc_u32 s1, s25, s1
	s_mov_b64 s[28:29], 0
	v_readlane_b32 s37, v254, 21
	v_readlane_b32 s38, v254, 22
	v_readlane_b32 s39, v254, 23
	v_readlane_b32 s40, v254, 24
	v_readlane_b32 s41, v254, 25
	v_readlane_b32 s42, v254, 26
	v_readlane_b32 s43, v254, 27
	v_readlane_b32 s44, v254, 28
	v_readlane_b32 s45, v254, 29
	v_readlane_b32 s46, v254, 30
	v_readlane_b32 s47, v254, 31
	v_readlane_b32 s48, v254, 32
	v_readlane_b32 s49, v254, 33

; #define G_SCHED __builtin_amdgcn_sched_barrier(0)
; #define CI_LOAD(R, kt) do { _Pragma("unroll") for (int _j = 0; _j < 16; ++_j) R[_j] = __builtin_nontemporal_load((const f32x4*)(src + (size_t)((kt) * 128 + _j) * LDB)); } while (0)
; template <int LDB>
; __device__ __forceinline__ void convert_image(const float* __restrict__ W, int col0, int col1, unsigned char* __restrict__ img, LAS3 char* lds, int wid) {
;     ...
;     f32x4 ra[16], rb[16];
;     CI_LOAD(ra, 0);
;     for (int kt = 0; kt < 16; kt += 2) {
;         CI_LOAD(rb, kt + 1); G_SCHED;
;         CI_CONV(ra, kt); G_SCHED;
.LBB0_490:
	v_add_co_u32_e32 v64, vcc, s19, v134
	s_add_i32 s13, s13, 2
	s_nop 0
	v_addc_co_u32_e32 v65, vcc, 0, v135, vcc
	v_add_co_u32_e32 v68, vcc, s7, v134
	s_nop 1
	v_addc_co_u32_e32 v69, vcc, 0, v135, vcc
	v_add_co_u32_e32 v72, vcc, s98, v134
	global_load_dwordx4 v[64:67], v[64:65], off nt
	s_nop 0
	global_load_dwordx4 v[68:71], v[68:69], off nt
	v_addc_co_u32_e32 v73, vcc, 0, v135, vcc
	v_add_co_u32_e32 v76, vcc, s9, v134
	s_nop 1
	v_addc_co_u32_e32 v77, vcc, 0, v135, vcc
	v_add_co_u32_e32 v80, vcc, s3, v134
	global_load_dwordx4 v[72:75], v[72:73], off nt
	s_nop 0
	global_load_dwordx4 v[76:79], v[76:77], off nt
	v_addc_co_u32_e32 v81, vcc, 0, v135, vcc
	v_add_co_u32_e32 v84, vcc, s18, v134
	s_nop 1
	v_addc_co_u32_e32 v85, vcc, 0, v135, vcc
	v_add_co_u32_e32 v88, vcc, s95, v134
	global_load_dwordx4 v[80:83], v[80:81], off nt
	s_nop 0
	global_load_dwordx4 v[84:87], v[84:85], off nt
	v_addc_co_u32_e32 v89, vcc, 0, v135, vcc
	v_add_co_u32_e32 v92, vcc, s31, v134
	s_nop 1
	v_addc_co_u32_e32 v93, vcc, 0, v135, vcc
	v_add_co_u32_e32 v96, vcc, s34, v134
	global_load_dwordx4 v[88:91], v[88:89], off nt
	s_nop 0
	global_load_dwordx4 v[92:95], v[92:93], off nt
	v_addc_co_u32_e32 v97, vcc, 0, v135, vcc
	v_add_co_u32_e32 v100, vcc, s35, v134
	s_nop 1
	v_addc_co_u32_e32 v101, vcc, 0, v135, vcc
	v_add_co_u32_e32 v104, vcc, s54, v134
	global_load_dwordx4 v[96:99], v[96:97], off nt
	s_nop 0
	global_load_dwordx4 v[100:103], v[100:101], off nt
	v_addc_co_u32_e32 v105, vcc, 0, v135, vcc
	v_add_co_u32_e32 v108, vcc, s55, v134
	s_nop 1
	v_addc_co_u32_e32 v109, vcc, 0, v135, vcc
	v_add_co_u32_e32 v112, vcc, s28, v134
	global_load_dwordx4 v[104:107], v[104:105], off nt
	s_nop 0
	global_load_dwordx4 v[108:111], v[108:109], off nt
	v_addc_co_u32_e32 v113, vcc, 0, v135, vcc
	v_add_co_u32_e32 v116, vcc, s29, v134
	s_nop 1
	v_addc_co_u32_e32 v117, vcc, 0, v135, vcc
	v_add_co_u32_e32 v120, vcc, s30, v134
	global_load_dwordx4 v[112:115], v[112:113], off nt
	s_nop 0
	global_load_dwordx4 v[116:119], v[116:117], off nt
	v_addc_co_u32_e32 v121, vcc, 0, v135, vcc
	global_load_dwordx4 v[128:131], v[134:135], off nt
	global_load_dwordx4 v[124:127], v[120:121], off nt
	v_add_u32_e32 v144, s76, v136
	v_mov_b32_e32 v152, v123
	v_mov_b32_e32 v153, v123
	v_mov_b32_e32 v154, v123
	v_mov_b32_e32 v155, v123
	s_cmp_lg_u32 s13, 0
	s_cbranch_scc1 .Lcw_gu
	s_waitcnt vmcnt(16)
.Lcw_gu:
	s_waitcnt vmcnt(34)
	v_cvt_scalef32_pk_fp8_f32 v152, v0, v4, s22
	s_waitcnt vmcnt(30)
	v_cvt_scalef32_pk_fp8_f32 v153, v16, v20, s22
	s_waitcnt vmcnt(26)
	v_cvt_scalef32_pk_fp8_f32 v154, v32, v36, s22
	s_waitcnt vmcnt(22)
	v_cvt_scalef32_pk_fp8_f32 v155, v48, v52, s22
	v_cvt_scalef32_pk_fp8_f32 v152, v8, v12, s22 op_sel:[0,0,0,1]
	v_cvt_scalef32_pk_fp8_f32 v153, v24, v28, s22 op_sel:[0,0,0,1]
	v_cvt_scalef32_pk_fp8_f32 v154, v40, v44, s22 op_sel:[0,0,0,1]
	s_waitcnt vmcnt(20)
	v_cvt_scalef32_pk_fp8_f32 v155, v56, v60, s22 op_sel:[0,0,0,1]
	ds_write_b128 v141, v[152:155]
	v_mov_b32_e32 v152, v123
	v_mov_b32_e32 v153, v123
	v_mov_b32_e32 v154, v123
	v_mov_b32_e32 v155, v123
	v_cvt_scalef32_pk_fp8_f32 v152, v1, v5, s22
	v_cvt_scalef32_pk_fp8_f32 v153, v17, v21, s22
	v_cvt_scalef32_pk_fp8_f32 v154, v33, v37, s22
	v_cvt_scalef32_pk_fp8_f32 v155, v49, v53, s22
	v_cvt_scalef32_pk_fp8_f32 v152, v9, v13, s22 op_sel:[0,0,0,1]
	v_cvt_scalef32_pk_fp8_f32 v153, v25, v29, s22 op_sel:[0,0,0,1]
	v_cvt_scalef32_pk_fp8_f32 v154, v41, v45, s22 op_sel:[0,0,0,1]
	v_cvt_scalef32_pk_fp8_f32 v155, v57, v61, s22 op_sel:[0,0,0,1]
	ds_write_b128 v141, v[152:155] offset:128
	v_mov_b32_e32 v152, v123
	v_mov_b32_e32 v0, v123
	v_cvt_scalef32_pk_fp8_f32 v152, v2, v6, s22
	v_mov_b32_e32 v153, v123
	v_mov_b32_e32 v154, v123
	v_mov_b32_e32 v155, v123
	v_cvt_scalef32_pk_fp8_f32 v0, v3, v7, s22
	v_mov_b32_e32 v1, v123
	v_mov_b32_e32 v2, v123
	v_mov_b32_e32 v3, v123
	v_cvt_scalef32_pk_fp8_f32 v153, v18, v22, s22
	v_cvt_scalef32_pk_fp8_f32 v154, v34, v38, s22
	v_cvt_scalef32_pk_fp8_f32 v155, v50, v54, s22
	v_cvt_scalef32_pk_fp8_f32 v1, v19, v23, s22
	v_cvt_scalef32_pk_fp8_f32 v2, v35, v39, s22
	v_cvt_scalef32_pk_fp8_f32 v3, v51, v55, s22
	v_cvt_scalef32_pk_fp8_f32 v152, v10, v14, s22 op_sel:[0,0,0,1]
	v_cvt_scalef32_pk_fp8_f32 v153, v26, v30, s22 op_sel:[0,0,0,1]
	v_cvt_scalef32_pk_fp8_f32 v154, v42, v46, s22 op_sel:[0,0,0,1]
	v_cvt_scalef32_pk_fp8_f32 v155, v58, v62, s22 op_sel:[0,0,0,1]
	v_cvt_scalef32_pk_fp8_f32 v0, v11, v15, s22 op_sel:[0,0,0,1]
	v_cvt_scalef32_pk_fp8_f32 v1, v27, v31, s22 op_sel:[0,0,0,1]
	v_cvt_scalef32_pk_fp8_f32 v2, v43, v47, s22 op_sel:[0,0,0,1]
	v_cvt_scalef32_pk_fp8_f32 v3, v59, v63, s22 op_sel:[0,0,0,1]
	ds_write_b128 v142, v[152:155]
	ds_write_b128 v143, v[0:3]
	s_waitcnt lgkmcnt(0)
	s_barrier
; #define G_SCHED __builtin_amdgcn_sched_barrier(0)
; #define CI_LOAD(R, kt) do { _Pragma("unroll") for (int _j = 0; _j < 16; ++_j) R[_j] = __builtin_nontemporal_load((const f32x4*)(src + (size_t)((kt) * 128 + _j) * LDB)); } while (0)
; template <int LDB>
; __device__ __forceinline__ void convert_image(const float* __restrict__ W, int col0, int col1, unsigned char* __restrict__ img, LAS3 char* lds, int wid) {
;     ...
;     f32x4 ra[16], rb[16];
;     CI_LOAD(ra, 0);
;     for (int kt = 0; kt < 16; kt += 2) {
;         CI_LOAD(rb, kt + 1); G_SCHED;
;         CI_CONV(ra, kt); G_SCHED;
;         CI_LOAD(ra, (kt + 2 < 16) ? kt + 2 : 15); G_SCHED;
;         CI_CONV(rb, kt + 1); G_SCHED;
	ds_read_b128 v[0:3], v144
	s_waitcnt lgkmcnt(0)
	s_nop 4
	global_store_dwordx4 v137, v[0:3], s[0:1] sc1
	s_nop 1
	ds_read_b128 v[0:3], v144 offset:1024
	s_waitcnt lgkmcnt(0)
	s_nop 4
	global_store_dwordx4 v138, v[0:3], s[0:1] sc1
	s_nop 1
	ds_read_b128 v[0:3], v144 offset:2048
	s_waitcnt lgkmcnt(0)
	s_nop 4
	global_store_dwordx4 v139, v[0:3], s[0:1] sc1
	s_nop 1
	ds_read_b128 v[0:3], v144 offset:3072
	s_waitcnt lgkmcnt(0)
	s_nop 4
	global_store_dwordx4 v140, v[0:3], s[0:1] sc1
	s_nop 1
	s_min_u32 s4, s13, 13
	s_lshl_b32 s4, s4, 21
	v_lshl_add_u64 v[56:57], v[132:133], 0, s[4:5]
	s_mov_b32 s4, 0x400000
	v_add_co_u32_e32 v0, vcc, s4, v56
	s_mov_b32 s4, 0x404000
	s_nop 0
	v_addc_co_u32_e32 v1, vcc, 0, v57, vcc
	v_add_co_u32_e32 v4, vcc, s4, v56
	s_mov_b32 s4, 0x408000
	s_nop 0
	v_addc_co_u32_e32 v5, vcc, 0, v57, vcc
	v_add_co_u32_e32 v8, vcc, s4, v56
	s_mov_b32 s4, 0x40c000
	s_nop 0
	v_addc_co_u32_e32 v9, vcc, 0, v57, vcc
	v_add_co_u32_e32 v12, vcc, s4, v56
	s_mov_b32 s4, 0x410000
	s_nop 0
	v_addc_co_u32_e32 v13, vcc, 0, v57, vcc
	v_add_co_u32_e32 v16, vcc, s4, v56
	s_mov_b32 s4, 0x414000
	s_nop 0
	v_addc_co_u32_e32 v17, vcc, 0, v57, vcc
	v_add_co_u32_e32 v20, vcc, s4, v56
	s_mov_b32 s4, 0x418000
	s_nop 0
	v_addc_co_u32_e32 v21, vcc, 0, v57, vcc
	v_add_co_u32_e32 v24, vcc, s4, v56
	s_mov_b32 s4, 0x41c000
	s_nop 0
	v_addc_co_u32_e32 v25, vcc, 0, v57, vcc
	v_add_co_u32_e32 v28, vcc, s4, v56
	s_mov_b32 s4, 0x420000
	s_nop 0
	v_addc_co_u32_e32 v29, vcc, 0, v57, vcc
	v_add_co_u32_e32 v32, vcc, s4, v56
	s_mov_b32 s4, 0x424000
	s_nop 0
	v_addc_co_u32_e32 v33, vcc, 0, v57, vcc
	v_add_co_u32_e32 v36, vcc, s4, v56
	s_mov_b32 s4, 0x428000
	s_nop 0
	v_addc_co_u32_e32 v37, vcc, 0, v57, vcc
	v_add_co_u32_e32 v40, vcc, s4, v56
	s_mov_b32 s4, 0x42c000
	s_nop 0
	v_addc_co_u32_e32 v41, vcc, 0, v57, vcc
	v_add_co_u32_e32 v44, vcc, s4, v56
	s_mov_b32 s4, 0x430000
	s_nop 0
	v_addc_co_u32_e32 v45, vcc, 0, v57, vcc
	v_add_co_u32_e32 v48, vcc, s4, v56
	s_mov_b32 s4, 0x434000
	s_nop 0
	v_addc_co_u32_e32 v49, vcc, 0, v57, vcc
	v_add_co_u32_e32 v52, vcc, s4, v56
	s_mov_b32 s4, 0x438000
	s_nop 0
	v_addc_co_u32_e32 v53, vcc, 0, v57, vcc
	v_add_co_u32_e32 v58, vcc, s4, v56
	s_mov_b32 s4, 0x43c000
	s_nop 0
	v_addc_co_u32_e32 v59, vcc, 0, v57, vcc
	v_add_co_u32_e32 v60, vcc, s4, v56
	global_load_dwordx4 v[0:3], v[0:1], off nt
	s_nop 0
	global_load_dwordx4 v[4:7], v[4:5], off nt
	v_addc_co_u32_e32 v61, vcc, 0, v57, vcc
	global_load_dwordx4 v[8:11], v[8:9], off nt
	s_nop 0
	global_load_dwordx4 v[12:15], v[12:13], off nt
	s_nop 0
	global_load_dwordx4 v[16:19], v[16:17], off nt
	s_nop 0
	global_load_dwordx4 v[20:23], v[20:21], off nt
	s_nop 0
	global_load_dwordx4 v[24:27], v[24:25], off nt
	s_nop 0
	global_load_dwordx4 v[28:31], v[28:29], off nt
	s_nop 0
	global_load_dwordx4 v[32:35], v[32:33], off nt
	s_nop 0
	global_load_dwordx4 v[36:39], v[36:37], off nt
	s_nop 0
	global_load_dwordx4 v[40:43], v[40:41], off nt
	s_nop 0
	global_load_dwordx4 v[44:47], v[44:45], off nt
	s_nop 0
	global_load_dwordx4 v[48:51], v[48:49], off nt
	s_nop 0
	global_load_dwordx4 v[52:55], v[52:53], off nt
	s_nop 0
	global_load_dwordx4 v[56:59], v[58:59], off nt
	s_nop 0
	global_load_dwordx4 v[60:63], v[60:61], off nt
	v_mov_b32_e32 v152, v123
	v_mov_b32_e32 v153, v123
	v_mov_b32_e32 v154, v123
	v_mov_b32_e32 v155, v123
	s_waitcnt vmcnt(21)
	v_cvt_scalef32_pk_fp8_f32 v152, v128, v64, s22
	v_cvt_scalef32_pk_fp8_f32 v153, v76, v80, s22
	v_cvt_scalef32_pk_fp8_f32 v154, v92, v96, s22
	v_cvt_scalef32_pk_fp8_f32 v155, v108, v112, s22
	v_cvt_scalef32_pk_fp8_f32 v152, v68, v72, s22 op_sel:[0,0,0,1]
	v_cvt_scalef32_pk_fp8_f32 v153, v84, v88, s22 op_sel:[0,0,0,1]
	v_cvt_scalef32_pk_fp8_f32 v154, v100, v104, s22 op_sel:[0,0,0,1]
	s_waitcnt vmcnt(20)
	v_cvt_scalef32_pk_fp8_f32 v155, v116, v124, s22 op_sel:[0,0,0,1]
	ds_write_b128 v141, v[152:155] offset:32768
	v_mov_b32_e32 v152, v123
	v_mov_b32_e32 v153, v123
	v_mov_b32_e32 v154, v123
	v_mov_b32_e32 v155, v123
	v_cvt_scalef32_pk_fp8_f32 v152, v129, v65, s22
	v_cvt_scalef32_pk_fp8_f32 v153, v77, v81, s22
	v_cvt_scalef32_pk_fp8_f32 v154, v93, v97, s22
	v_cvt_scalef32_pk_fp8_f32 v155, v109, v113, s22
	v_cvt_scalef32_pk_fp8_f32 v152, v69, v73, s22 op_sel:[0,0,0,1]
	v_cvt_scalef32_pk_fp8_f32 v153, v85, v89, s22 op_sel:[0,0,0,1]
	v_cvt_scalef32_pk_fp8_f32 v154, v101, v105, s22 op_sel:[0,0,0,1]
	v_cvt_scalef32_pk_fp8_f32 v155, v117, v125, s22 op_sel:[0,0,0,1]
	ds_write_b128 v141, v[152:155] offset:32896
	v_mov_b32_e32 v152, v123
	v_mov_b32_e32 v153, v123
	v_mov_b32_e32 v154, v123
	v_mov_b32_e32 v155, v123
	v_mov_b32_e32 v120, v123
	v_mov_b32_e32 v121, v123
	v_mov_b32_e32 v122, v123
	v_cvt_scalef32_pk_fp8_f32 v152, v130, v66, s22
	v_cvt_scalef32_pk_fp8_f32 v153, v78, v82, s22
	v_cvt_scalef32_pk_fp8_f32 v154, v94, v98, s22
	v_cvt_scalef32_pk_fp8_f32 v155, v110, v114, s22
	v_cvt_scalef32_pk_fp8_f32 v120, v131, v67, s22
	v_cvt_scalef32_pk_fp8_f32 v121, v79, v83, s22
	v_cvt_scalef32_pk_fp8_f32 v122, v95, v99, s22
	v_cvt_scalef32_pk_fp8_f32 v123, v111, v115, s22
	v_cvt_scalef32_pk_fp8_f32 v152, v70, v74, s22 op_sel:[0,0,0,1]
	v_cvt_scalef32_pk_fp8_f32 v153, v86, v90, s22 op_sel:[0,0,0,1]
	v_cvt_scalef32_pk_fp8_f32 v154, v102, v106, s22 op_sel:[0,0,0,1]
	v_cvt_scalef32_pk_fp8_f32 v155, v118, v126, s22 op_sel:[0,0,0,1]
	v_cvt_scalef32_pk_fp8_f32 v120, v71, v75, s22 op_sel:[0,0,0,1]
	v_cvt_scalef32_pk_fp8_f32 v121, v87, v91, s22 op_sel:[0,0,0,1]
	v_cvt_scalef32_pk_fp8_f32 v122, v103, v107, s22 op_sel:[0,0,0,1]
	v_cvt_scalef32_pk_fp8_f32 v123, v119, v127, s22 op_sel:[0,0,0,1]
	s_add_u32 s24, s0, 0x8000
	ds_write_b128 v142, v[152:155] offset:32768
	ds_write_b128 v143, v[120:123] offset:32768
	s_waitcnt lgkmcnt(0)
	s_barrier
	ds_read_b128 v[64:67], v144 offset:32768
	s_addc_u32 s25, s1, 0
	s_waitcnt lgkmcnt(0)
	s_nop 4
	global_store_dwordx4 v137, v[64:67], s[24:25] sc1
	s_nop 1
	ds_read_b128 v[64:67], v144 offset:33792
	s_waitcnt lgkmcnt(0)
	s_nop 4
	global_store_dwordx4 v138, v[64:67], s[24:25] sc1
	s_nop 1
	ds_read_b128 v[64:67], v144 offset:34816
	s_waitcnt lgkmcnt(0)
	s_nop 4
	global_store_dwordx4 v139, v[64:67], s[24:25] sc1
	s_nop 1
	ds_read_b128 v[64:67], v144 offset:35840
	s_waitcnt lgkmcnt(0)
	s_nop 4
	global_store_dwordx4 v140, v[64:67], s[24:25] sc1
	s_nop 1
	s_add_u32 s0, s0, 0x10000
	s_addc_u32 s1, s1, 0
	s_mov_b64 s[24:25], 0x400000
	s_cmp_lt_u32 s13, 14
	v_lshl_add_u64 v[134:135], v[134:135], 0, s[24:25]
	s_cbranch_scc1 .LBB0_490

; #define LAS3 __attribute__((address_space(3)))
; template <int EPI>
; __device__ __forceinline__ void gemm_tile_img(const GemmArgs& g, int pm, int pn, int e, int ebase, int ecnt, LAS3 char* lds, int wid, const unsigned char* img, const TileSync& sy, int kh = -1) {
;     ...
;         for (int bj = 0; bj < 2; ++bj)
; #pragma unroll
;             for (int n = 0; n < 2; ++n) bv[bj][n] = *(LAS3 const f32x4*)(lds + LDS_BIAS + (bj * 128 + n * 64 + colw) * 4);
; #pragma unroll
;         for (int ai = 0; ai < 2; ++ai)
; #pragma unroll
;             for (int m = 0; m < 4; ++m) {
;                 LAS3 char* rp = lds + (ai * 128 + row0 + m * 16) * EST_F8W + colw;
; #pragma unroll
;                 for (int bj = 0; bj < 2; ++bj)
; #pragma unroll
;                     for (int n = 0; n < 2; ++n) { const f32x4 v = acc[ai][bj][m][n] + bv[bj][n];
;                         int w = __builtin_amdgcn_cvt_pk_fp8_f32(v[0], v[1], 0, false); w = __builtin_amdgcn_cvt_pk_fp8_f32(v[2], v[3], w, true);
;                         *(LAS3 int*)(rp + bj * 128 + n * 64) = w; }
;             }
.LBB0_567:
	s_or_b64 exec, exec, s[0:1]
	v_lshrrev_b32_e32 v151, 2, v149
	v_and_b32_e32 v152, 60, v151
	v_lshl_add_u32 v0, v152, 2, 0
	v_add_u32_e32 v1, 0x21c00, v0
	v_add_u32_e32 v2, 0x21d00, v0
	ds_read_b128 v[140:143], v1
	ds_read_b128 v[136:139], v2
	v_mov_b32_e32 v153, 0
	v_add_u32_e32 v1, 0x21e00, v0
	v_add_u32_e32 v0, 0x21f00, v0
	s_waitcnt lgkmcnt(1)
	v_pk_add_f32 v[132:133], v[132:133], v[140:141]
	s_waitcnt lgkmcnt(0)
	v_pk_add_f32 v[128:129], v[128:129], v[136:137]
	v_cvt_pk_fp8_f32 v153, v132, v133
	v_mov_b32_e32 v132, 0
	ds_read_b128 v[4:7], v1
	ds_read_b128 v[0:3], v0
	v_cvt_pk_fp8_f32 v132, v128, v129
	v_pk_add_f32 v[128:129], v[134:135], v[142:143]
	v_and_b32_e32 v150, 15, v149
	v_cvt_pk_fp8_f32 v153, v128, v129 op_sel:[0,0,1]
	v_pk_add_f32 v[128:129], v[130:131], v[138:139]
	s_waitcnt lgkmcnt(1)
	v_pk_add_f32 v[120:121], v[120:121], v[4:5]
	v_cvt_pk_fp8_f32 v132, v128, v129 op_sel:[0,0,1]
	v_mov_b32_e32 v129, 0
	v_cvt_pk_fp8_f32 v129, v120, v121
	s_waitcnt lgkmcnt(0)
	v_pk_add_f32 v[112:113], v[112:113], v[0:1]
	v_mov_b32_e32 v120, 0
	v_cvt_pk_fp8_f32 v120, v112, v113
	v_pk_add_f32 v[112:113], v[122:123], v[6:7]
	v_pk_add_f32 v[104:105], v[104:105], v[4:5]
	v_cvt_pk_fp8_f32 v129, v112, v113 op_sel:[0,0,1]
	v_pk_add_f32 v[112:113], v[114:115], v[2:3]
	v_mov_b32_e32 v114, 0
	v_cvt_pk_fp8_f32 v120, v112, v113 op_sel:[0,0,1]
	v_pk_add_f32 v[112:113], v[124:125], v[140:141]
	v_mov_b32_e32 v115, 0
	v_cvt_pk_fp8_f32 v114, v112, v113
	v_pk_add_f32 v[112:113], v[116:117], v[136:137]
	v_pk_add_f32 v[96:97], v[96:97], v[0:1]
	v_cvt_pk_fp8_f32 v115, v112, v113
	v_pk_add_f32 v[112:113], v[126:127], v[142:143]
	s_mov_b32 s0, 0xfffffc0
	v_cvt_pk_fp8_f32 v114, v112, v113 op_sel:[0,0,1]
	v_pk_add_f32 v[112:113], v[118:119], v[138:139]
	v_and_or_b32 v128, v151, s0, v150
	v_cvt_pk_fp8_f32 v115, v112, v113 op_sel:[0,0,1]
	v_mov_b32_e32 v112, 0
	v_cvt_pk_fp8_f32 v112, v104, v105
	v_mov_b32_e32 v104, 0
	v_cvt_pk_fp8_f32 v104, v96, v97
	v_pk_add_f32 v[96:97], v[106:107], v[6:7]
	v_mul_lo_u32 v128, v128, s34
	v_cvt_pk_fp8_f32 v112, v96, v97 op_sel:[0,0,1]
	v_pk_add_f32 v[96:97], v[98:99], v[2:3]
	v_add3_u32 v128, 0, v152, v128
	v_cvt_pk_fp8_f32 v104, v96, v97 op_sel:[0,0,1]
	v_add_u32_e32 v96, 0x1000, v128
	ds_write2_b32 v128, v153, v132 offset1:16
	ds_write2_b32 v128, v129, v120 offset0:32 offset1:48
	ds_write2_b32 v96, v114, v115 offset0:64 offset1:80
	ds_write2_b32 v96, v112, v104 offset0:96 offset1:112
	v_pk_add_f32 v[96:97], v[108:109], v[140:141]
	v_mov_b32_e32 v98, 0
	v_cvt_pk_fp8_f32 v98, v96, v97
	v_pk_add_f32 v[96:97], v[100:101], v[136:137]
	v_mov_b32_e32 v99, 0
	v_cvt_pk_fp8_f32 v99, v96, v97
	v_pk_add_f32 v[96:97], v[110:111], v[142:143]
	v_pk_add_f32 v[88:89], v[88:89], v[4:5]
	v_cvt_pk_fp8_f32 v98, v96, v97 op_sel:[0,0,1]
	v_pk_add_f32 v[96:97], v[102:103], v[138:139]
	v_pk_add_f32 v[80:81], v[80:81], v[0:1]
	v_cvt_pk_fp8_f32 v99, v96, v97 op_sel:[0,0,1]
	v_mov_b32_e32 v97, 0
	v_cvt_pk_fp8_f32 v97, v88, v89
	v_mov_b32_e32 v88, 0
	v_cvt_pk_fp8_f32 v88, v80, v81
	v_pk_add_f32 v[80:81], v[90:91], v[6:7]
	v_pk_add_f32 v[76:77], v[76:77], v[4:5]
	v_cvt_pk_fp8_f32 v97, v80, v81 op_sel:[0,0,1]
	v_pk_add_f32 v[80:81], v[82:83], v[2:3]
	v_mov_b32_e32 v82, 0
	v_cvt_pk_fp8_f32 v88, v80, v81 op_sel:[0,0,1]
	v_pk_add_f32 v[80:81], v[92:93], v[140:141]
	v_mov_b32_e32 v83, 0
	v_cvt_pk_fp8_f32 v82, v80, v81
	v_pk_add_f32 v[80:81], v[84:85], v[136:137]
	v_pk_add_f32 v[72:73], v[72:73], v[0:1]
	v_cvt_pk_fp8_f32 v83, v80, v81
	v_pk_add_f32 v[80:81], v[94:95], v[142:143]
	v_pk_add_f32 v[68:69], v[68:69], v[140:141]
	v_cvt_pk_fp8_f32 v82, v80, v81 op_sel:[0,0,1]
	v_pk_add_f32 v[80:81], v[86:87], v[138:139]
	v_pk_add_f32 v[64:65], v[64:65], v[136:137]
	v_cvt_pk_fp8_f32 v83, v80, v81 op_sel:[0,0,1]
	v_mov_b32_e32 v81, 0
	v_cvt_pk_fp8_f32 v81, v76, v77
	v_mov_b32_e32 v76, 0
	v_cvt_pk_fp8_f32 v76, v72, v73
	v_pk_add_f32 v[72:73], v[78:79], v[6:7]
	v_pk_add_f32 v[56:57], v[56:57], v[4:5]
	v_cvt_pk_fp8_f32 v81, v72, v73 op_sel:[0,0,1]
	v_pk_add_f32 v[72:73], v[74:75], v[2:3]
	v_pk_add_f32 v[48:49], v[48:49], v[0:1]
	v_cvt_pk_fp8_f32 v76, v72, v73 op_sel:[0,0,1]
	v_mov_b32_e32 v72, 0
	v_cvt_pk_fp8_f32 v72, v68, v69
	v_mov_b32_e32 v68, 0
	v_cvt_pk_fp8_f32 v68, v64, v65
	v_pk_add_f32 v[64:65], v[70:71], v[142:143]
; #define LAS3 __attribute__((address_space(3)))
; #define LD_WAIT(r) asm volatile("s_waitcnt vmcnt(0)" : "+v"(r) :: "memory")
; template <int EPI>
; __device__ __forceinline__ void gemm_tile_img(const GemmArgs& g, int pm, int pn, int e, int ebase, int ecnt, LAS3 char* lds, int wid, const unsigned char* img, const TileSync& sy, int kh = -1) {
;     ...
;                 LAS3 char* rp = lds + (ai * 128 + row0 + m * 16) * EST_F8W + colw;
; #pragma unroll
;                 for (int bj = 0; bj < 2; ++bj)
; #pragma unroll
;                     for (int n = 0; n < 2; ++n) { const f32x4 v = acc[ai][bj][m][n] + bv[bj][n];
;                         int w = __builtin_amdgcn_cvt_pk_fp8_f32(v[0], v[1], 0, false); w = __builtin_amdgcn_cvt_pk_fp8_f32(v[2], v[3], w, true);
;                         *(LAS3 int*)(rp + bj * 128 + n * 64) = w; }
;             }
;         { const int nv = ecnt - pm * 256; epi_flush_f8w((unsigned char*)g.C, D, ebase + pm * 256, pn * 256, nv < 256 ? nv : 256, lds, tz); }
;     ...
;     if (EPI >= 2 && tz == 0) { LD_WAIT(nx); *sy.qslot = sy.qtag | nx; }
	v_add_u32_e32 v96, 0x2000, v128
	v_cvt_pk_fp8_f32 v72, v64, v65 op_sel:[0,0,1]
	v_pk_add_f32 v[64:65], v[66:67], v[138:139]
	v_add_u32_e32 v80, 0x3000, v128
	v_cvt_pk_fp8_f32 v68, v64, v65 op_sel:[0,0,1]
	v_mov_b32_e32 v64, 0
	v_cvt_pk_fp8_f32 v64, v56, v57
	v_mov_b32_e32 v56, 0
	v_cvt_pk_fp8_f32 v56, v48, v49
	v_pk_add_f32 v[48:49], v[58:59], v[6:7]
	ds_write2_b32 v96, v98, v99 offset0:128 offset1:144
	ds_write2_b32 v96, v97, v88 offset0:160 offset1:176
	v_cvt_pk_fp8_f32 v64, v48, v49 op_sel:[0,0,1]
	v_pk_add_f32 v[48:49], v[50:51], v[2:3]
	ds_write2_b32 v80, v82, v83 offset0:192 offset1:208
	v_cvt_pk_fp8_f32 v56, v48, v49 op_sel:[0,0,1]
	v_add_u32_e32 v48, 0x8800, v128
	ds_write2_b32 v80, v81, v76 offset0:224 offset1:240
	ds_write2_b32 v48, v72, v68 offset1:16
	ds_write2_b32 v48, v64, v56 offset0:32 offset1:48
	v_pk_add_f32 v[48:49], v[60:61], v[140:141]
	v_mov_b32_e32 v50, 0
	v_cvt_pk_fp8_f32 v50, v48, v49
	v_pk_add_f32 v[48:49], v[52:53], v[136:137]
	v_mov_b32_e32 v51, 0
	v_cvt_pk_fp8_f32 v51, v48, v49
	v_pk_add_f32 v[48:49], v[62:63], v[142:143]
	v_pk_add_f32 v[36:37], v[36:37], v[4:5]
	v_cvt_pk_fp8_f32 v50, v48, v49 op_sel:[0,0,1]
	v_pk_add_f32 v[48:49], v[54:55], v[138:139]
	v_pk_add_f32 v[32:33], v[32:33], v[0:1]
	v_cvt_pk_fp8_f32 v51, v48, v49 op_sel:[0,0,1]
	v_mov_b32_e32 v49, 0
	v_cvt_pk_fp8_f32 v49, v36, v37
	v_mov_b32_e32 v36, 0
	v_cvt_pk_fp8_f32 v36, v32, v33
	v_pk_add_f32 v[32:33], v[38:39], v[6:7]
	v_pk_add_f32 v[20:21], v[20:21], v[4:5]
	v_cvt_pk_fp8_f32 v49, v32, v33 op_sel:[0,0,1]
	v_pk_add_f32 v[32:33], v[34:35], v[2:3]
	v_mov_b32_e32 v34, 0
	v_cvt_pk_fp8_f32 v36, v32, v33 op_sel:[0,0,1]
	v_pk_add_f32 v[32:33], v[44:45], v[140:141]
	v_mov_b32_e32 v35, 0
	v_cvt_pk_fp8_f32 v34, v32, v33
	v_pk_add_f32 v[32:33], v[40:41], v[136:137]
	v_pk_add_f32 v[16:17], v[16:17], v[0:1]
	v_cvt_pk_fp8_f32 v35, v32, v33
	v_pk_add_f32 v[32:33], v[46:47], v[142:143]
	v_pk_add_f32 v[4:5], v[12:13], v[4:5]
	v_cvt_pk_fp8_f32 v34, v32, v33 op_sel:[0,0,1]
	v_pk_add_f32 v[32:33], v[42:43], v[138:139]
	v_mov_b32_e32 v12, 0
	v_cvt_pk_fp8_f32 v35, v32, v33 op_sel:[0,0,1]
	v_mov_b32_e32 v33, 0
	v_cvt_pk_fp8_f32 v33, v20, v21
	v_mov_b32_e32 v20, 0
	v_cvt_pk_fp8_f32 v20, v16, v17
	v_pk_add_f32 v[16:17], v[22:23], v[6:7]
	v_cvt_pk_fp8_f32 v12, v4, v5
	v_cvt_pk_fp8_f32 v33, v16, v17 op_sel:[0,0,1]
	v_pk_add_f32 v[16:17], v[18:19], v[2:3]
	v_mov_b32_e32 v18, 0
	v_cvt_pk_fp8_f32 v20, v16, v17 op_sel:[0,0,1]
	v_pk_add_f32 v[16:17], v[28:29], v[140:141]
	v_mov_b32_e32 v19, 0
	v_cvt_pk_fp8_f32 v18, v16, v17
	v_pk_add_f32 v[16:17], v[24:25], v[136:137]
	v_pk_add_f32 v[0:1], v[8:9], v[0:1]
	v_cvt_pk_fp8_f32 v19, v16, v17
	v_mov_b32_e32 v4, 0
	v_cvt_pk_fp8_f32 v4, v0, v1
	v_pk_add_f32 v[16:17], v[30:31], v[142:143]
	v_pk_add_f32 v[0:1], v[14:15], v[6:7]
	v_cvt_pk_fp8_f32 v18, v16, v17 op_sel:[0,0,1]
	v_pk_add_f32 v[16:17], v[26:27], v[138:139]
	v_cvt_pk_fp8_f32 v12, v0, v1 op_sel:[0,0,1]
	v_cvt_pk_fp8_f32 v19, v16, v17 op_sel:[0,0,1]
	v_pk_add_f32 v[0:1], v[10:11], v[2:3]
	v_add_u32_e32 v48, 0x9800, v128
	v_cvt_pk_fp8_f32 v4, v0, v1 op_sel:[0,0,1]
	v_add_u32_e32 v32, 0xa800, v128
	v_add_u32_e32 v0, 0xb800, v128
	s_lshl_b32 s0, s24, 8
	ds_write2_b32 v48, v50, v51 offset0:64 offset1:80
	ds_write2_b32 v48, v49, v36 offset0:96 offset1:112
	ds_write2_b32 v32, v34, v35 offset0:128 offset1:144
	ds_write2_b32 v32, v33, v20 offset0:160 offset1:176
	ds_write2_b32 v0, v18, v19 offset0:192 offset1:208
	ds_write2_b32 v0, v12, v4 offset0:224 offset1:240
	s_sub_i32 s1, s13, s0
	v_lshlrev_b32_e32 v0, 4, v149
	s_min_i32 s25, s1, 0x100
	v_ashrrev_i32_e32 v2, 4, v149
	v_and_b32_e32 v1, 0xf0, v0
	s_add_i32 s4, s62, s0
	v_add_u32_e32 v0, 0, v1
	v_lshl_or_b32 v1, s15, 8, v1
	v_cmp_gt_i32_e64 s[0:1], s25, v2
	s_waitcnt lgkmcnt(0)
	s_barrier
	s_and_saveexec_b64 s[30:31], vcc
	s_cbranch_execz .Ltk_dn
	v_readlane_b32 s11, v255, 12
	s_waitcnt vmcnt(0)
	s_nop 1
	v_mov_b32_e32 v9, s35
	v_or_b32_e32 v8, s11, v148
	ds_write_b32 v9, v8
.Ltk_dn:
	s_or_b64 exec, exec, s[30:31]
	s_and_saveexec_b64 s[30:31], s[0:1]
	v_readlane_b32 s11, v255, 12
	s_cbranch_execz .LBB0_569
	v_mad_u64_u32 v[4:5], s[0:1], v2, s34, v[0:1]
	v_add_u32_e32 v3, s4, v2
	ds_read_b128 v[4:7], v4
	v_lshl_or_b32 v3, v3, 11, v1
	s_waitcnt lgkmcnt(0)
	s_nop 4
	global_store_dwordx4 v3, v[4:7], s[66:67] nt
	s_nop 1

; #define LD_WAIT(r) asm volatile("s_waitcnt vmcnt(0)" : "+v"(r) :: "memory")
; __device__ __forceinline__ void epi_flush_f8w(unsigned char* C, size_t ld, int grow0, int col0, int nvalid, LAS3 char* lds, int tid) {
;     ...
;             asm volatile("s_nop 4\n\tglobal_store_dwordx4 %0, %1, %2 nt\n\ts_nop 1" :: "v"(off), "v"(q), "s"(C) : "memory"); } }
;     __syncthreads();
; template <int EPI>
; __device__ __forceinline__ void gemm_tile_img(const GemmArgs& g, int pm, int pn, int e, int ebase, int ecnt, LAS3 char* lds, int wid, const unsigned char* img, const TileSync& sy, int kh = -1) {
;     ...
;     if (EPI >= 2 && tz == 0) { LD_WAIT(nx); *sy.qslot = sy.qtag | nx; }
.LBB0_583:
	s_or_b64 exec, exec, s[30:31]
	s_barrier
	s_and_saveexec_b64 s[0:1], vcc
	s_cbranch_execz .LBB0_585
.LBB0_585:
	s_or_b64 exec, exec, s[0:1]
	s_mov_b64 s[0:1], 0

; #define G_SCHED __builtin_amdgcn_sched_barrier(0)
; #define CI_LOAD(R, kt) do { _Pragma("unroll") for (int _j = 0; _j < 16; ++_j) R[_j] = __builtin_nontemporal_load((const f32x4*)(src + (size_t)((kt) * 128 + _j) * LDB)); } while (0)
; template <int LDB>
; __device__ __forceinline__ void convert_image(const float* __restrict__ W, int col0, int col1, unsigned char* __restrict__ img, LAS3 char* lds, int wid) {
;     ...
;     f32x4 ra[16], rb[16];
;     CI_LOAD(ra, 0);
;     for (int kt = 0; kt < 16; kt += 2) {
;         CI_LOAD(rb, kt + 1); G_SCHED;
;         CI_CONV(ra, kt); G_SCHED;
.LBB0_589:
	v_add_co_u32_e32 v64, vcc, s20, v134
	s_add_i32 s14, s14, 2
	s_nop 0
	v_addc_co_u32_e32 v65, vcc, 0, v135, vcc
	v_add_co_u32_e32 v68, vcc, s21, v134
	s_nop 1
	v_addc_co_u32_e32 v69, vcc, 0, v135, vcc
	v_add_co_u32_e32 v72, vcc, s22, v134
	global_load_dwordx4 v[64:67], v[64:65], off nt
	s_nop 0
	global_load_dwordx4 v[68:71], v[68:69], off nt
	v_addc_co_u32_e32 v73, vcc, 0, v135, vcc
	v_add_co_u32_e32 v76, vcc, s23, v134
	s_nop 1
	v_addc_co_u32_e32 v77, vcc, 0, v135, vcc
	v_add_co_u32_e32 v80, vcc, s86, v134
	global_load_dwordx4 v[72:75], v[72:73], off nt
	s_nop 0
	global_load_dwordx4 v[76:79], v[76:77], off nt
	v_addc_co_u32_e32 v81, vcc, 0, v135, vcc
	v_add_co_u32_e32 v84, vcc, s87, v134
	s_nop 1
	v_addc_co_u32_e32 v85, vcc, 0, v135, vcc
	v_add_co_u32_e32 v88, vcc, s95, v134
	global_load_dwordx4 v[80:83], v[80:81], off nt
	s_nop 0
	global_load_dwordx4 v[84:87], v[84:85], off nt
	v_addc_co_u32_e32 v89, vcc, 0, v135, vcc
	v_add_co_u32_e32 v92, vcc, s8, v134
	s_nop 1
	v_addc_co_u32_e32 v93, vcc, 0, v135, vcc
	v_add_co_u32_e32 v96, vcc, s97, v134
	global_load_dwordx4 v[88:91], v[88:89], off nt
	s_nop 0
	global_load_dwordx4 v[92:95], v[92:93], off nt
	v_addc_co_u32_e32 v97, vcc, 0, v135, vcc
	v_add_co_u32_e32 v100, vcc, s98, v134
	s_nop 1
	v_addc_co_u32_e32 v101, vcc, 0, v135, vcc
	v_add_co_u32_e32 v104, vcc, s99, v134
	global_load_dwordx4 v[96:99], v[96:97], off nt
	s_nop 0
	global_load_dwordx4 v[100:103], v[100:101], off nt
	v_addc_co_u32_e32 v105, vcc, 0, v135, vcc
	v_add_co_u32_e32 v108, vcc, s18, v134
	s_nop 1
	v_addc_co_u32_e32 v109, vcc, 0, v135, vcc
	v_add_co_u32_e32 v112, vcc, s7, v134
	global_load_dwordx4 v[104:107], v[104:105], off nt
	s_nop 0
	global_load_dwordx4 v[108:111], v[108:109], off nt
	v_addc_co_u32_e32 v113, vcc, 0, v135, vcc
	v_add_co_u32_e32 v116, vcc, s9, v134
	s_nop 1
	v_addc_co_u32_e32 v117, vcc, 0, v135, vcc
	v_add_co_u32_e32 v120, vcc, s16, v134
	global_load_dwordx4 v[112:115], v[112:113], off nt
	s_nop 0
	global_load_dwordx4 v[116:119], v[116:117], off nt
	v_addc_co_u32_e32 v121, vcc, 0, v135, vcc
	global_load_dwordx4 v[128:131], v[134:135], off nt
	global_load_dwordx4 v[124:127], v[120:121], off nt
	v_add_u32_e32 v152, s76, v136
	v_mov_b32_e32 v148, v123
	v_mov_b32_e32 v149, v123
	v_mov_b32_e32 v150, v123
	v_mov_b32_e32 v151, v123
	s_cmp_lg_u32 s14, 0
	s_cbranch_scc1 .Lcw_dn
	s_waitcnt vmcnt(16)
.Lcw_dn:
	s_waitcnt vmcnt(34)
	v_cvt_scalef32_pk_fp8_f32 v148, v0, v4, s17
	s_waitcnt vmcnt(30)
	v_cvt_scalef32_pk_fp8_f32 v149, v16, v20, s17
	s_waitcnt vmcnt(26)
	v_cvt_scalef32_pk_fp8_f32 v150, v32, v36, s17
	s_waitcnt vmcnt(22)
	v_cvt_scalef32_pk_fp8_f32 v151, v48, v52, s17
	v_cvt_scalef32_pk_fp8_f32 v148, v8, v12, s17 op_sel:[0,0,0,1]
	v_cvt_scalef32_pk_fp8_f32 v149, v24, v28, s17 op_sel:[0,0,0,1]
	v_cvt_scalef32_pk_fp8_f32 v150, v40, v44, s17 op_sel:[0,0,0,1]
	s_waitcnt vmcnt(20)
	v_cvt_scalef32_pk_fp8_f32 v151, v56, v60, s17 op_sel:[0,0,0,1]
	ds_write_b128 v141, v[148:151]
	v_mov_b32_e32 v148, v123
	v_mov_b32_e32 v149, v123
	v_mov_b32_e32 v150, v123
	v_mov_b32_e32 v151, v123
	v_cvt_scalef32_pk_fp8_f32 v148, v1, v5, s17
	v_cvt_scalef32_pk_fp8_f32 v149, v17, v21, s17
	v_cvt_scalef32_pk_fp8_f32 v150, v33, v37, s17
	v_cvt_scalef32_pk_fp8_f32 v151, v49, v53, s17
	v_cvt_scalef32_pk_fp8_f32 v148, v9, v13, s17 op_sel:[0,0,0,1]
	v_cvt_scalef32_pk_fp8_f32 v149, v25, v29, s17 op_sel:[0,0,0,1]
	v_cvt_scalef32_pk_fp8_f32 v150, v41, v45, s17 op_sel:[0,0,0,1]
	v_cvt_scalef32_pk_fp8_f32 v151, v57, v61, s17 op_sel:[0,0,0,1]
	ds_write_b128 v141, v[148:151] offset:128
	v_mov_b32_e32 v148, v123
	v_mov_b32_e32 v0, v123
	v_cvt_scalef32_pk_fp8_f32 v148, v2, v6, s17
	v_mov_b32_e32 v149, v123
	v_mov_b32_e32 v150, v123
	v_mov_b32_e32 v151, v123
	v_cvt_scalef32_pk_fp8_f32 v0, v3, v7, s17
	v_mov_b32_e32 v1, v123
	v_mov_b32_e32 v2, v123
	v_mov_b32_e32 v3, v123
	v_cvt_scalef32_pk_fp8_f32 v149, v18, v22, s17
	v_cvt_scalef32_pk_fp8_f32 v150, v34, v38, s17
	v_cvt_scalef32_pk_fp8_f32 v151, v50, v54, s17
	v_cvt_scalef32_pk_fp8_f32 v1, v19, v23, s17
	v_cvt_scalef32_pk_fp8_f32 v2, v35, v39, s17
	v_cvt_scalef32_pk_fp8_f32 v3, v51, v55, s17
	v_cvt_scalef32_pk_fp8_f32 v148, v10, v14, s17 op_sel:[0,0,0,1]
	v_cvt_scalef32_pk_fp8_f32 v149, v26, v30, s17 op_sel:[0,0,0,1]
	v_cvt_scalef32_pk_fp8_f32 v150, v42, v46, s17 op_sel:[0,0,0,1]
	v_cvt_scalef32_pk_fp8_f32 v151, v58, v62, s17 op_sel:[0,0,0,1]
	v_cvt_scalef32_pk_fp8_f32 v0, v11, v15, s17 op_sel:[0,0,0,1]
	v_cvt_scalef32_pk_fp8_f32 v1, v27, v31, s17 op_sel:[0,0,0,1]
	v_cvt_scalef32_pk_fp8_f32 v2, v43, v47, s17 op_sel:[0,0,0,1]
	v_cvt_scalef32_pk_fp8_f32 v3, v59, v63, s17 op_sel:[0,0,0,1]
	ds_write_b128 v142, v[148:151]
	ds_write_b128 v143, v[0:3]
	s_waitcnt lgkmcnt(0)
	s_barrier
; #define G_SCHED __builtin_amdgcn_sched_barrier(0)
; #define CI_LOAD(R, kt) do { _Pragma("unroll") for (int _j = 0; _j < 16; ++_j) R[_j] = __builtin_nontemporal_load((const f32x4*)(src + (size_t)((kt) * 128 + _j) * LDB)); } while (0)
; template <int LDB>
; __device__ __forceinline__ void convert_image(const float* __restrict__ W, int col0, int col1, unsigned char* __restrict__ img, LAS3 char* lds, int wid) {
;     ...
;     f32x4 ra[16], rb[16];
;     CI_LOAD(ra, 0);
;     for (int kt = 0; kt < 16; kt += 2) {
;         CI_LOAD(rb, kt + 1); G_SCHED;
;         CI_CONV(ra, kt); G_SCHED;
;         CI_LOAD(ra, (kt + 2 < 16) ? kt + 2 : 15); G_SCHED;
;         CI_CONV(rb, kt + 1); G_SCHED;
;     }
;     asm volatile("s_waitcnt vmcnt(0)" ::: "memory");
;     __syncthreads();
	ds_read_b128 v[0:3], v152
	s_waitcnt lgkmcnt(0)
	s_nop 4
	global_store_dwordx4 v137, v[0:3], s[0:1] sc1
	s_nop 1
	ds_read_b128 v[0:3], v152 offset:1024
	s_waitcnt lgkmcnt(0)
	s_nop 4
	global_store_dwordx4 v138, v[0:3], s[0:1] sc1
	s_nop 1
	ds_read_b128 v[0:3], v152 offset:2048
	s_waitcnt lgkmcnt(0)
	s_nop 4
	global_store_dwordx4 v139, v[0:3], s[0:1] sc1
	s_nop 1
	ds_read_b128 v[0:3], v152 offset:3072
	s_waitcnt lgkmcnt(0)
	s_nop 4
	global_store_dwordx4 v140, v[0:3], s[0:1] sc1
	s_nop 1
	s_min_u32 s4, s14, 13
	s_lshl_b32 s4, s4, 20
	v_lshl_add_u64 v[56:57], v[132:133], 0, s[4:5]
	s_mov_b32 s4, 0x200000
	v_add_co_u32_e32 v0, vcc, s4, v56
	s_mov_b32 s4, 0x202000
	s_nop 0
	v_addc_co_u32_e32 v1, vcc, 0, v57, vcc
	v_add_co_u32_e32 v4, vcc, s4, v56
	s_mov_b32 s4, 0x204000
	s_nop 0
	v_addc_co_u32_e32 v5, vcc, 0, v57, vcc
	v_add_co_u32_e32 v8, vcc, s4, v56
	s_mov_b32 s4, 0x206000
	s_nop 0
	v_addc_co_u32_e32 v9, vcc, 0, v57, vcc
	v_add_co_u32_e32 v12, vcc, s4, v56
	s_mov_b32 s4, 0x208000
	s_nop 0
	v_addc_co_u32_e32 v13, vcc, 0, v57, vcc
	v_add_co_u32_e32 v16, vcc, s4, v56
	s_mov_b32 s4, 0x20a000
	s_nop 0
	v_addc_co_u32_e32 v17, vcc, 0, v57, vcc
	v_add_co_u32_e32 v20, vcc, s4, v56
	s_mov_b32 s4, 0x20c000
	s_nop 0
	v_addc_co_u32_e32 v21, vcc, 0, v57, vcc
	v_add_co_u32_e32 v24, vcc, s4, v56
	s_mov_b32 s4, 0x20e000
	s_nop 0
	v_addc_co_u32_e32 v25, vcc, 0, v57, vcc
	v_add_co_u32_e32 v28, vcc, s4, v56
	s_mov_b32 s4, 0x210000
	s_nop 0
	v_addc_co_u32_e32 v29, vcc, 0, v57, vcc
	v_add_co_u32_e32 v32, vcc, s4, v56
	s_mov_b32 s4, 0x212000
	s_nop 0
	v_addc_co_u32_e32 v33, vcc, 0, v57, vcc
	v_add_co_u32_e32 v36, vcc, s4, v56
	s_mov_b32 s4, 0x214000
	s_nop 0
	v_addc_co_u32_e32 v37, vcc, 0, v57, vcc
	v_add_co_u32_e32 v40, vcc, s4, v56
	s_mov_b32 s4, 0x216000
	s_nop 0
	v_addc_co_u32_e32 v41, vcc, 0, v57, vcc
	v_add_co_u32_e32 v44, vcc, s4, v56
	s_mov_b32 s4, 0x218000
	s_nop 0
	v_addc_co_u32_e32 v45, vcc, 0, v57, vcc
	v_add_co_u32_e32 v48, vcc, s4, v56
	s_mov_b32 s4, 0x21a000
	s_nop 0
	v_addc_co_u32_e32 v49, vcc, 0, v57, vcc
	v_add_co_u32_e32 v52, vcc, s4, v56
	s_mov_b32 s4, 0x21c000
	s_nop 0
	v_addc_co_u32_e32 v53, vcc, 0, v57, vcc
	v_add_co_u32_e32 v58, vcc, s4, v56
	s_mov_b32 s4, 0x21e000
	s_nop 0
	v_addc_co_u32_e32 v59, vcc, 0, v57, vcc
	v_add_co_u32_e32 v60, vcc, s4, v56
	global_load_dwordx4 v[0:3], v[0:1], off nt
	s_nop 0
	global_load_dwordx4 v[4:7], v[4:5], off nt
	v_addc_co_u32_e32 v61, vcc, 0, v57, vcc
	global_load_dwordx4 v[8:11], v[8:9], off nt
	s_nop 0
	global_load_dwordx4 v[12:15], v[12:13], off nt
	s_nop 0
	global_load_dwordx4 v[16:19], v[16:17], off nt
	s_nop 0
	global_load_dwordx4 v[20:23], v[20:21], off nt
	s_nop 0
	global_load_dwordx4 v[24:27], v[24:25], off nt
	s_nop 0
	global_load_dwordx4 v[28:31], v[28:29], off nt
	s_nop 0
	global_load_dwordx4 v[32:35], v[32:33], off nt
	s_nop 0
	global_load_dwordx4 v[36:39], v[36:37], off nt
	s_nop 0
	global_load_dwordx4 v[40:43], v[40:41], off nt
	s_nop 0
	global_load_dwordx4 v[44:47], v[44:45], off nt
	s_nop 0
	global_load_dwordx4 v[48:51], v[48:49], off nt
	s_nop 0
	global_load_dwordx4 v[52:55], v[52:53], off nt
	s_nop 0
	global_load_dwordx4 v[56:59], v[58:59], off nt
	s_nop 0
	global_load_dwordx4 v[60:63], v[60:61], off nt
	v_mov_b32_e32 v148, v123
	v_mov_b32_e32 v149, v123
	v_mov_b32_e32 v150, v123
	v_mov_b32_e32 v151, v123
	s_waitcnt vmcnt(21)
	v_cvt_scalef32_pk_fp8_f32 v148, v128, v64, s17
	v_cvt_scalef32_pk_fp8_f32 v149, v76, v80, s17
	v_cvt_scalef32_pk_fp8_f32 v150, v92, v96, s17
	v_cvt_scalef32_pk_fp8_f32 v151, v108, v112, s17
	v_cvt_scalef32_pk_fp8_f32 v148, v68, v72, s17 op_sel:[0,0,0,1]
	v_cvt_scalef32_pk_fp8_f32 v149, v84, v88, s17 op_sel:[0,0,0,1]
	v_cvt_scalef32_pk_fp8_f32 v150, v100, v104, s17 op_sel:[0,0,0,1]
	s_waitcnt vmcnt(20)
	v_cvt_scalef32_pk_fp8_f32 v151, v116, v124, s17 op_sel:[0,0,0,1]
	ds_write_b128 v141, v[148:151] offset:32768
	v_mov_b32_e32 v148, v123
	v_mov_b32_e32 v149, v123
	v_mov_b32_e32 v150, v123
	v_mov_b32_e32 v151, v123
	v_cvt_scalef32_pk_fp8_f32 v148, v129, v65, s17
	v_cvt_scalef32_pk_fp8_f32 v149, v77, v81, s17
	v_cvt_scalef32_pk_fp8_f32 v150, v93, v97, s17
	v_cvt_scalef32_pk_fp8_f32 v151, v109, v113, s17
	v_cvt_scalef32_pk_fp8_f32 v148, v69, v73, s17 op_sel:[0,0,0,1]
	v_cvt_scalef32_pk_fp8_f32 v149, v85, v89, s17 op_sel:[0,0,0,1]
	v_cvt_scalef32_pk_fp8_f32 v150, v101, v105, s17 op_sel:[0,0,0,1]
	v_cvt_scalef32_pk_fp8_f32 v151, v117, v125, s17 op_sel:[0,0,0,1]
	ds_write_b128 v141, v[148:151] offset:32896
	v_mov_b32_e32 v148, v123
	v_mov_b32_e32 v149, v123
	v_mov_b32_e32 v150, v123
	v_mov_b32_e32 v151, v123
	v_mov_b32_e32 v120, v123
	v_mov_b32_e32 v121, v123
	v_mov_b32_e32 v122, v123
	v_cvt_scalef32_pk_fp8_f32 v148, v130, v66, s17
	v_cvt_scalef32_pk_fp8_f32 v149, v78, v82, s17
	v_cvt_scalef32_pk_fp8_f32 v150, v94, v98, s17
	v_cvt_scalef32_pk_fp8_f32 v151, v110, v114, s17
	v_cvt_scalef32_pk_fp8_f32 v120, v131, v67, s17
	v_cvt_scalef32_pk_fp8_f32 v121, v79, v83, s17
	v_cvt_scalef32_pk_fp8_f32 v122, v95, v99, s17
	v_cvt_scalef32_pk_fp8_f32 v123, v111, v115, s17
	v_cvt_scalef32_pk_fp8_f32 v148, v70, v74, s17 op_sel:[0,0,0,1]
	v_cvt_scalef32_pk_fp8_f32 v149, v86, v90, s17 op_sel:[0,0,0,1]
	v_cvt_scalef32_pk_fp8_f32 v150, v102, v106, s17 op_sel:[0,0,0,1]
	v_cvt_scalef32_pk_fp8_f32 v151, v118, v126, s17 op_sel:[0,0,0,1]
	v_cvt_scalef32_pk_fp8_f32 v120, v71, v75, s17 op_sel:[0,0,0,1]
	v_cvt_scalef32_pk_fp8_f32 v121, v87, v91, s17 op_sel:[0,0,0,1]
	v_cvt_scalef32_pk_fp8_f32 v122, v103, v107, s17 op_sel:[0,0,0,1]
	v_cvt_scalef32_pk_fp8_f32 v123, v119, v127, s17 op_sel:[0,0,0,1]
	s_add_u32 s30, s0, 0x8000
	ds_write_b128 v142, v[148:151] offset:32768
	ds_write_b128 v143, v[120:123] offset:32768
	s_waitcnt lgkmcnt(0)
	s_barrier
	ds_read_b128 v[64:67], v152 offset:32768
	s_addc_u32 s31, s1, 0
	s_waitcnt lgkmcnt(0)
	s_nop 4
	global_store_dwordx4 v137, v[64:67], s[30:31] sc1
	s_nop 1
	ds_read_b128 v[64:67], v152 offset:33792
	s_waitcnt lgkmcnt(0)
	s_nop 4
	global_store_dwordx4 v138, v[64:67], s[30:31] sc1
	s_nop 1
	ds_read_b128 v[64:67], v152 offset:34816
	s_waitcnt lgkmcnt(0)
	s_nop 4
	global_store_dwordx4 v139, v[64:67], s[30:31] sc1
	s_nop 1
	ds_read_b128 v[64:67], v152 offset:35840
	s_waitcnt lgkmcnt(0)
	s_nop 4
	global_store_dwordx4 v140, v[64:67], s[30:31] sc1
	s_nop 1
	s_add_u32 s0, s0, 0x10000
	s_addc_u32 s1, s1, 0
	s_mov_b64 s[30:31], 0x200000
	s_cmp_lt_u32 s14, 14
	v_lshl_add_u64 v[134:135], v[134:135], 0, s[30:31]
	s_cbranch_scc1 .LBB0_589
	s_waitcnt vmcnt(0)
	s_barrier
